# all four GEMM K-loops: stage pieces addressed by SGPR pair + lane offset (64-bit VALU address adds replaced by SALU)
# speedup vs baseline: 1.0041x; 1.0041x over previous
.LBB0_243:
	s_add_u32 s75, s6, 0x100
	s_addc_u32 s48, s7, 0
	s_lshl_b32 s49, s45, 8
	s_lshl_b32 s8, s45, 20
	s_bitset1_b32 s49, 7
	s_mov_b32 s80, -2
	s_mov_b64 s[6:7], 0
	s_cmp_eq_u32 s80, 28
	s_cselect_b64 s[34:35], -1, 0
	s_and_b64 s[24:25], s[0:1], s[34:35]
	s_andn2_b64 vcc, exec, s[24:25]
	v_mov_b32_e32 v128, v170
	v_mov_b32_e32 v129, v160
	s_add_u32 vcc_lo, s70, s6
	s_addc_u32 vcc_hi, s71, s7
	s_add_u32 s81, vcc_lo, 0x32000100
	s_addc_u32 s50, vcc_hi, 0
	s_and_b64 s[24:25], s[34:35], exec
	s_cselect_b32 s25, s73, s50
	s_cselect_b32 s24, s72, s81
	s_add_u32 s50, s75, s6
	s_addc_u32 s51, s48, s7
	s_and_b64 s[34:35], s[34:35], exec
	s_cselect_b32 s35, s79, s51
	s_cselect_b32 s34, s78, s50
	s_add_i32 s50, 0, 0x10000
	s_add_i32 s51, 0, 0x14000
	v_add_u32_e32 v142, s50, v177
	v_add_u32_e32 v158, s51, v177
	ds_read_b128 v[130:133], v142
	ds_read_b128 v[134:137], v213
	ds_read_b128 v[138:141], v142 offset:2048
	ds_read_b128 v[142:145], v213 offset:2048
	ds_read_b128 v[146:149], v158
	ds_read_b128 v[150:153], v213 offset:16384
	ds_read_b128 v[154:157], v158 offset:2048
	ds_read_b128 v[172:175], v213 offset:18432
	ds_read_b128 v[180:183], v178
	ds_read_b128 v[184:187], v212
	ds_read_b128 v[188:191], v178 offset:2048
	ds_read_b128 v[192:195], v212 offset:2048
	ds_read_b128 v[196:199], v178 offset:4096
	ds_read_b128 v[200:203], v212 offset:4096
	ds_read_b128 v[204:207], v178 offset:6144
	ds_read_b128 v[208:211], v212 offset:6144
	s_add_i32 m0, s97, 0xc000
	s_add_u32 vcc_lo, vcc_lo, s54
	s_addc_u32 vcc_hi, vcc_hi, s55
	v_mov_b32_e32 v171, v161
	global_load_lds_dwordx4 v160, vcc
	s_add_i32 m0, s97, 0xe000
	s_nop 0
	global_load_lds_dwordx4 v170, vcc
	s_waitcnt vmcnt(8)
	s_waitcnt lgkmcnt(0)
	s_barrier
	s_setprio 1
	s_waitcnt lgkmcnt(0)
	v_mfma_f32_16x16x32_bf16 v[100:103], v[130:133], v[180:183], 0
	v_mfma_f32_16x16x32_bf16 v[96:99], v[138:141], v[180:183], 0
	v_mfma_f32_16x16x32_bf16 v[92:95], v[130:133], v[188:191], 0
	v_mfma_f32_16x16x32_bf16 v[88:91], v[138:141], v[188:191], 0
	v_mfma_f32_16x16x32_bf16 v[84:87], v[130:133], v[196:199], 0
	v_mfma_f32_16x16x32_bf16 v[80:83], v[138:141], v[196:199], 0
	v_mfma_f32_16x16x32_bf16 v[76:79], v[130:133], v[204:207], 0
	v_mfma_f32_16x16x32_bf16 v[72:75], v[138:141], v[204:207], 0
	v_mfma_f32_16x16x32_bf16 v[100:103], v[134:137], v[184:187], v[100:103]
	v_mfma_f32_16x16x32_bf16 v[96:99], v[142:145], v[184:187], v[96:99]
	v_mfma_f32_16x16x32_bf16 v[92:95], v[134:137], v[192:195], v[92:95]
	v_mfma_f32_16x16x32_bf16 v[88:91], v[142:145], v[192:195], v[88:91]
	v_mfma_f32_16x16x32_bf16 v[84:87], v[134:137], v[200:203], v[84:87]
	v_mfma_f32_16x16x32_bf16 v[80:83], v[142:145], v[200:203], v[80:83]
	v_mfma_f32_16x16x32_bf16 v[76:79], v[134:137], v[208:211], v[76:79]
	v_mfma_f32_16x16x32_bf16 v[72:75], v[142:145], v[208:211], v[72:75]
	s_setprio 0
	s_setprio 1
	v_mfma_f32_16x16x32_bf16 v[68:71], v[146:149], v[180:183], 0
	v_mfma_f32_16x16x32_bf16 v[64:67], v[154:157], v[180:183], 0
	v_mfma_f32_16x16x32_bf16 v[60:63], v[146:149], v[188:191], 0
	v_mfma_f32_16x16x32_bf16 v[56:59], v[154:157], v[188:191], 0
	v_mfma_f32_16x16x32_bf16 v[52:55], v[146:149], v[196:199], 0
	v_mfma_f32_16x16x32_bf16 v[48:51], v[154:157], v[196:199], 0
	v_mfma_f32_16x16x32_bf16 v[40:43], v[146:149], v[204:207], 0
	v_mfma_f32_16x16x32_bf16 v[32:35], v[154:157], v[204:207], 0
	v_mfma_f32_16x16x32_bf16 v[68:71], v[150:153], v[184:187], v[68:71]
	v_mfma_f32_16x16x32_bf16 v[64:67], v[172:175], v[184:187], v[64:67]
	v_mfma_f32_16x16x32_bf16 v[60:63], v[150:153], v[192:195], v[60:63]
	v_mfma_f32_16x16x32_bf16 v[56:59], v[172:175], v[192:195], v[56:59]
	v_mfma_f32_16x16x32_bf16 v[52:55], v[150:153], v[200:203], v[52:55]
	v_mfma_f32_16x16x32_bf16 v[48:51], v[172:175], v[200:203], v[48:51]
	v_mfma_f32_16x16x32_bf16 v[40:43], v[150:153], v[208:211], v[40:43]
	v_mfma_f32_16x16x32_bf16 v[32:35], v[172:175], v[208:211], v[32:35]
	s_setprio 0
	s_barrier
	s_add_i32 s50, s50, s61
	s_mov_b32 m0, s50
	ds_read_b128 v[180:183], v178 offset:16384
	ds_read_b128 v[184:187], v212 offset:16384
	ds_read_b128 v[188:191], v178 offset:18432
	ds_read_b128 v[192:195], v212 offset:18432
	ds_read_b128 v[196:199], v178 offset:20480
	ds_read_b128 v[200:203], v212 offset:20480
	ds_read_b128 v[204:207], v178 offset:22528
	ds_read_b128 v[208:211], v212 offset:22528
	s_nop 0
	global_load_lds_dwordx4 v168, s[34:35]
	s_add_i32 m0, s50, 0x2000
	s_add_u32 vcc_lo, s34, 0x8000
	s_addc_u32 vcc_hi, s35, 0
	s_add_i32 s50, s51, s61
	s_nop 0
	global_load_lds_dwordx4 v162, s[34:35]
	s_mov_b32 m0, s50
	s_nop 0
	global_load_lds_dwordx4 v168, vcc
	s_add_i32 m0, s50, 0x2000
	s_nop 0
	global_load_lds_dwordx4 v162, vcc
	s_waitcnt vmcnt(6)
	s_waitcnt lgkmcnt(0)
	s_barrier
	s_setprio 1
	s_waitcnt lgkmcnt(0)
	v_mfma_f32_16x16x32_bf16 v[44:47], v[130:133], v[180:183], 0
	v_mfma_f32_16x16x32_bf16 v[36:39], v[138:141], v[180:183], 0
	v_mfma_f32_16x16x32_bf16 v[28:31], v[130:133], v[188:191], 0
	v_mfma_f32_16x16x32_bf16 v[24:27], v[138:141], v[188:191], 0
	v_mfma_f32_16x16x32_bf16 v[20:23], v[130:133], v[196:199], 0
	v_mfma_f32_16x16x32_bf16 v[16:19], v[138:141], v[196:199], 0
	v_mfma_f32_16x16x32_bf16 v[12:15], v[130:133], v[204:207], 0
	v_mfma_f32_16x16x32_bf16 v[8:11], v[138:141], v[204:207], 0
	v_mfma_f32_16x16x32_bf16 v[44:47], v[134:137], v[184:187], v[44:47]
	v_mfma_f32_16x16x32_bf16 v[36:39], v[142:145], v[184:187], v[36:39]
	v_mfma_f32_16x16x32_bf16 v[28:31], v[134:137], v[192:195], v[28:31]
	v_mfma_f32_16x16x32_bf16 v[24:27], v[142:145], v[192:195], v[24:27]
	v_mfma_f32_16x16x32_bf16 v[20:23], v[134:137], v[200:203], v[20:23]
	v_mfma_f32_16x16x32_bf16 v[16:19], v[142:145], v[200:203], v[16:19]
	v_mfma_f32_16x16x32_bf16 v[12:15], v[134:137], v[208:211], v[12:15]
	v_mfma_f32_16x16x32_bf16 v[8:11], v[142:145], v[208:211], v[8:11]
	s_setprio 0
	s_setprio 1
	v_mfma_f32_16x16x32_bf16 v[4:7], v[146:149], v[180:183], 0
	v_mfma_f32_16x16x32_bf16 v[0:3], v[154:157], v[180:183], 0
	v_mfma_f32_16x16x32_bf16 v[104:107], v[146:149], v[188:191], 0
	v_mfma_f32_16x16x32_bf16 v[108:111], v[154:157], v[188:191], 0
	v_mfma_f32_16x16x32_bf16 v[112:115], v[146:149], v[196:199], 0
	v_mfma_f32_16x16x32_bf16 v[116:119], v[154:157], v[196:199], 0
	v_mfma_f32_16x16x32_bf16 v[120:123], v[146:149], v[204:207], 0
	v_mfma_f32_16x16x32_bf16 v[124:127], v[154:157], v[204:207], 0
	v_mfma_f32_16x16x32_bf16 v[4:7], v[150:153], v[184:187], v[4:7]
	v_mfma_f32_16x16x32_bf16 v[0:3], v[172:175], v[184:187], v[0:3]
	v_mfma_f32_16x16x32_bf16 v[104:107], v[150:153], v[192:195], v[104:107]
	v_mfma_f32_16x16x32_bf16 v[108:111], v[172:175], v[192:195], v[108:111]
	v_mfma_f32_16x16x32_bf16 v[112:115], v[150:153], v[200:203], v[112:115]
	v_mfma_f32_16x16x32_bf16 v[116:119], v[172:175], v[200:203], v[116:119]
	v_mfma_f32_16x16x32_bf16 v[120:123], v[150:153], v[208:211], v[120:123]
	v_mfma_f32_16x16x32_bf16 v[124:127], v[172:175], v[208:211], v[124:127]
	s_setprio 0
	s_barrier
	s_add_i32 s50, 0, 0x18000
	s_add_i32 s51, 0, 0x1c000
	v_add_u32_e32 v142, s50, v177
	v_add_u32_e32 v158, s51, v177
	ds_read_b128 v[130:133], v142
	ds_read_b128 v[134:137], v213 offset:32768
	ds_read_b128 v[138:141], v142 offset:2048
	ds_read_b128 v[142:145], v213 offset:34816
	ds_read_b128 v[146:149], v158
	ds_read_b128 v[150:153], v213 offset:49152
	ds_read_b128 v[154:157], v158 offset:2048
	ds_read_b128 v[172:175], v213 offset:51200
	s_mov_b32 m0, s29
	v_mov_b32_e32 v160, v129
	ds_read_b128 v[180:183], v178 offset:32768
	ds_read_b128 v[184:187], v212 offset:32768
	ds_read_b128 v[188:191], v178 offset:34816
	ds_read_b128 v[192:195], v212 offset:34816
	ds_read_b128 v[196:199], v178 offset:36864
	ds_read_b128 v[200:203], v212 offset:36864
	ds_read_b128 v[204:207], v178 offset:38912
	ds_read_b128 v[208:211], v212 offset:38912
	s_mov_b32 m0, s97
	s_nop 0
	global_load_lds_dwordx4 v164, s[24:25]
	s_mov_b32 m0, s28
	s_nop 0
	global_load_lds_dwordx4 v166, s[24:25]
	s_mov_b32 m0, s29
	v_mov_b32_e32 v170, v128
	global_load_lds_dwordx4 v160, s[24:25]
	s_mov_b32 m0, s30
	s_nop 0
	global_load_lds_dwordx4 v170, s[24:25]
	s_waitcnt vmcnt(8)
	s_waitcnt lgkmcnt(0)
	s_barrier
	s_setprio 1
	s_waitcnt lgkmcnt(0)
	v_mfma_f32_16x16x32_bf16 v[100:103], v[130:133], v[180:183], v[100:103]
	v_mfma_f32_16x16x32_bf16 v[96:99], v[138:141], v[180:183], v[96:99]
	v_mfma_f32_16x16x32_bf16 v[92:95], v[130:133], v[188:191], v[92:95]
	v_mfma_f32_16x16x32_bf16 v[88:91], v[138:141], v[188:191], v[88:91]
	v_mfma_f32_16x16x32_bf16 v[84:87], v[130:133], v[196:199], v[84:87]
	v_mfma_f32_16x16x32_bf16 v[80:83], v[138:141], v[196:199], v[80:83]
	v_mfma_f32_16x16x32_bf16 v[76:79], v[130:133], v[204:207], v[76:79]
	v_mfma_f32_16x16x32_bf16 v[72:75], v[138:141], v[204:207], v[72:75]
	v_mfma_f32_16x16x32_bf16 v[100:103], v[134:137], v[184:187], v[100:103]
	v_mfma_f32_16x16x32_bf16 v[96:99], v[142:145], v[184:187], v[96:99]
	v_mfma_f32_16x16x32_bf16 v[92:95], v[134:137], v[192:195], v[92:95]
	v_mfma_f32_16x16x32_bf16 v[88:91], v[142:145], v[192:195], v[88:91]
	v_mfma_f32_16x16x32_bf16 v[84:87], v[134:137], v[200:203], v[84:87]
	v_mfma_f32_16x16x32_bf16 v[80:83], v[142:145], v[200:203], v[80:83]
	v_mfma_f32_16x16x32_bf16 v[76:79], v[134:137], v[208:211], v[76:79]
	v_mfma_f32_16x16x32_bf16 v[72:75], v[142:145], v[208:211], v[72:75]
	s_setprio 0
	s_setprio 1
	v_mfma_f32_16x16x32_bf16 v[68:71], v[146:149], v[180:183], v[68:71]
	v_mfma_f32_16x16x32_bf16 v[64:67], v[154:157], v[180:183], v[64:67]
	v_mfma_f32_16x16x32_bf16 v[60:63], v[146:149], v[188:191], v[60:63]
	v_mfma_f32_16x16x32_bf16 v[56:59], v[154:157], v[188:191], v[56:59]
	v_mfma_f32_16x16x32_bf16 v[52:55], v[146:149], v[196:199], v[52:55]
	v_mfma_f32_16x16x32_bf16 v[48:51], v[154:157], v[196:199], v[48:51]
	v_mfma_f32_16x16x32_bf16 v[40:43], v[146:149], v[204:207], v[40:43]
	v_mfma_f32_16x16x32_bf16 v[32:35], v[154:157], v[204:207], v[32:35]
	v_mfma_f32_16x16x32_bf16 v[68:71], v[150:153], v[184:187], v[68:71]
	v_mfma_f32_16x16x32_bf16 v[64:67], v[172:175], v[184:187], v[64:67]
	v_mfma_f32_16x16x32_bf16 v[60:63], v[150:153], v[192:195], v[60:63]
	v_mfma_f32_16x16x32_bf16 v[56:59], v[172:175], v[192:195], v[56:59]
	v_mfma_f32_16x16x32_bf16 v[52:55], v[150:153], v[200:203], v[52:55]
	v_mfma_f32_16x16x32_bf16 v[48:51], v[172:175], v[200:203], v[48:51]
	v_mfma_f32_16x16x32_bf16 v[40:43], v[150:153], v[208:211], v[40:43]
	v_mfma_f32_16x16x32_bf16 v[32:35], v[172:175], v[208:211], v[32:35]
	s_setprio 0
	s_barrier
	v_mov_b32_e32 v169, v161
	ds_read_b128 v[180:183], v178 offset:49152
	ds_read_b128 v[184:187], v212 offset:49152
	ds_read_b128 v[188:191], v178 offset:51200
	ds_read_b128 v[192:195], v212 offset:51200
	ds_read_b128 v[196:199], v178 offset:53248
	ds_read_b128 v[200:203], v212 offset:53248
	ds_read_b128 v[204:207], v178 offset:55296
	ds_read_b128 v[208:211], v212 offset:55296
	s_add_i32 s50, s50, s61
	s_add_u32 vcc_lo, s34, s52
	s_addc_u32 vcc_hi, s35, s53
	s_mov_b32 m0, s50
	v_mov_b32_e32 v163, v161
	global_load_lds_dwordx4 v168, vcc
	s_add_i32 m0, s50, 0x2000
	v_mov_b32_e32 v165, v161
	s_add_u32 s34, s34, 0x8080
	s_addc_u32 s35, s35, 0
	s_add_i32 s50, s51, s61
	global_load_lds_dwordx4 v162, vcc
	s_mov_b32 m0, s50
	v_mov_b32_e32 v167, v161
	global_load_lds_dwordx4 v168, s[34:35]
	s_add_i32 m0, s50, 0x2000
	s_nop 0
	global_load_lds_dwordx4 v162, s[34:35]
	s_mov_b32 m0, s31
	s_add_u32 vcc_lo, s24, s52
	s_addc_u32 vcc_hi, s25, s53
	global_load_lds_dwordx4 v164, vcc
	s_mov_b32 m0, s42
	s_nop 0
	global_load_lds_dwordx4 v166, vcc
	s_waitcnt vmcnt(8)
	s_waitcnt lgkmcnt(0)
	s_barrier
	s_setprio 1
	s_waitcnt lgkmcnt(0)
	v_mfma_f32_16x16x32_bf16 v[44:47], v[130:133], v[180:183], v[44:47]
	v_mfma_f32_16x16x32_bf16 v[36:39], v[138:141], v[180:183], v[36:39]
	v_mfma_f32_16x16x32_bf16 v[28:31], v[130:133], v[188:191], v[28:31]
	v_mfma_f32_16x16x32_bf16 v[24:27], v[138:141], v[188:191], v[24:27]
	v_mfma_f32_16x16x32_bf16 v[20:23], v[130:133], v[196:199], v[20:23]
	v_mfma_f32_16x16x32_bf16 v[16:19], v[138:141], v[196:199], v[16:19]
	v_mfma_f32_16x16x32_bf16 v[12:15], v[130:133], v[204:207], v[12:15]
	v_mfma_f32_16x16x32_bf16 v[8:11], v[138:141], v[204:207], v[8:11]
	v_mfma_f32_16x16x32_bf16 v[44:47], v[134:137], v[184:187], v[44:47]
	v_mfma_f32_16x16x32_bf16 v[36:39], v[142:145], v[184:187], v[36:39]
	v_mfma_f32_16x16x32_bf16 v[28:31], v[134:137], v[192:195], v[28:31]
	v_mfma_f32_16x16x32_bf16 v[24:27], v[142:145], v[192:195], v[24:27]
	v_mfma_f32_16x16x32_bf16 v[20:23], v[134:137], v[200:203], v[20:23]
	v_mfma_f32_16x16x32_bf16 v[16:19], v[142:145], v[200:203], v[16:19]
	v_mfma_f32_16x16x32_bf16 v[12:15], v[134:137], v[208:211], v[12:15]
	v_mfma_f32_16x16x32_bf16 v[8:11], v[142:145], v[208:211], v[8:11]
	s_setprio 0
	s_setprio 1
	v_mfma_f32_16x16x32_bf16 v[4:7], v[146:149], v[180:183], v[4:7]
	v_mfma_f32_16x16x32_bf16 v[0:3], v[154:157], v[180:183], v[0:3]
	v_mfma_f32_16x16x32_bf16 v[104:107], v[146:149], v[188:191], v[104:107]
	v_mfma_f32_16x16x32_bf16 v[108:111], v[154:157], v[188:191], v[108:111]
	v_mfma_f32_16x16x32_bf16 v[112:115], v[146:149], v[196:199], v[112:115]
	v_mfma_f32_16x16x32_bf16 v[116:119], v[154:157], v[196:199], v[116:119]
	v_mfma_f32_16x16x32_bf16 v[120:123], v[146:149], v[204:207], v[120:123]
	v_mfma_f32_16x16x32_bf16 v[124:127], v[154:157], v[204:207], v[124:127]
	v_mfma_f32_16x16x32_bf16 v[4:7], v[150:153], v[184:187], v[4:7]
	v_mfma_f32_16x16x32_bf16 v[0:3], v[172:175], v[184:187], v[0:3]
	v_mfma_f32_16x16x32_bf16 v[104:107], v[150:153], v[192:195], v[104:107]
	v_mfma_f32_16x16x32_bf16 v[108:111], v[172:175], v[192:195], v[108:111]
	v_mfma_f32_16x16x32_bf16 v[112:115], v[150:153], v[200:203], v[112:115]
	v_mfma_f32_16x16x32_bf16 v[116:119], v[172:175], v[200:203], v[116:119]
	v_mfma_f32_16x16x32_bf16 v[120:123], v[150:153], v[208:211], v[120:123]
	v_mfma_f32_16x16x32_bf16 v[124:127], v[172:175], v[208:211], v[124:127]
	s_setprio 0
	s_barrier
	s_add_i32 s80, s80, 2
	s_add_u32 s6, s6, 0x100
	s_addc_u32 s7, s7, 0
	s_branch .LBB0_245
.LBB0_244:
	s_add_u32 vcc_lo, s70, s6
	s_addc_u32 vcc_hi, s71, s7
	s_add_u32 s81, vcc_lo, 0x32000100
	s_addc_u32 s50, vcc_hi, 0
	s_and_b64 s[24:25], s[34:35], exec
	s_cselect_b32 s25, s73, s50
	s_cselect_b32 s24, s72, s81
	s_add_u32 s50, s75, s6
	s_addc_u32 s51, s48, s7
	s_and_b64 s[34:35], s[34:35], exec
	s_cselect_b32 s35, s79, s51
	s_cselect_b32 s34, s78, s50
	s_add_i32 s50, 0, 0x10000
	s_add_i32 s51, 0, 0x14000
	v_add_u32_e32 v142, s50, v177
	v_add_u32_e32 v158, s51, v177
	ds_read_b128 v[130:133], v142
	ds_read_b128 v[134:137], v213
	ds_read_b128 v[138:141], v142 offset:2048
	ds_read_b128 v[142:145], v213 offset:2048
	ds_read_b128 v[146:149], v158
	ds_read_b128 v[150:153], v213 offset:16384
	ds_read_b128 v[154:157], v158 offset:2048
	ds_read_b128 v[172:175], v213 offset:18432
	ds_read_b128 v[180:183], v178
	ds_read_b128 v[184:187], v212
	ds_read_b128 v[188:191], v178 offset:2048
	ds_read_b128 v[192:195], v212 offset:2048
	ds_read_b128 v[196:199], v178 offset:4096
	ds_read_b128 v[200:203], v212 offset:4096
	ds_read_b128 v[204:207], v178 offset:6144
	ds_read_b128 v[208:211], v212 offset:6144
	s_add_i32 m0, s97, 0xc000
	s_add_u32 vcc_lo, vcc_lo, s54
	s_addc_u32 vcc_hi, vcc_hi, s55
	v_mov_b32_e32 v171, v161
	global_load_lds_dwordx4 v160, vcc
	s_add_i32 m0, s97, 0xe000
	s_nop 0
	global_load_lds_dwordx4 v170, vcc
	s_waitcnt vmcnt(8)
	s_waitcnt lgkmcnt(0)
	s_barrier
	s_setprio 1
	s_waitcnt lgkmcnt(0)
	v_mfma_f32_16x16x32_bf16 v[100:103], v[130:133], v[180:183], v[100:103]
	v_mfma_f32_16x16x32_bf16 v[96:99], v[138:141], v[180:183], v[96:99]
	v_mfma_f32_16x16x32_bf16 v[92:95], v[130:133], v[188:191], v[92:95]
	v_mfma_f32_16x16x32_bf16 v[88:91], v[138:141], v[188:191], v[88:91]
	v_mfma_f32_16x16x32_bf16 v[84:87], v[130:133], v[196:199], v[84:87]
	v_mfma_f32_16x16x32_bf16 v[80:83], v[138:141], v[196:199], v[80:83]
	v_mfma_f32_16x16x32_bf16 v[76:79], v[130:133], v[204:207], v[76:79]
	v_mfma_f32_16x16x32_bf16 v[72:75], v[138:141], v[204:207], v[72:75]
	v_mfma_f32_16x16x32_bf16 v[100:103], v[134:137], v[184:187], v[100:103]
	v_mfma_f32_16x16x32_bf16 v[96:99], v[142:145], v[184:187], v[96:99]
	v_mfma_f32_16x16x32_bf16 v[92:95], v[134:137], v[192:195], v[92:95]
	v_mfma_f32_16x16x32_bf16 v[88:91], v[142:145], v[192:195], v[88:91]
	v_mfma_f32_16x16x32_bf16 v[84:87], v[134:137], v[200:203], v[84:87]
	v_mfma_f32_16x16x32_bf16 v[80:83], v[142:145], v[200:203], v[80:83]
	v_mfma_f32_16x16x32_bf16 v[76:79], v[134:137], v[208:211], v[76:79]
	v_mfma_f32_16x16x32_bf16 v[72:75], v[142:145], v[208:211], v[72:75]
	s_setprio 0
	s_setprio 1
	v_mfma_f32_16x16x32_bf16 v[68:71], v[146:149], v[180:183], v[68:71]
	v_mfma_f32_16x16x32_bf16 v[64:67], v[154:157], v[180:183], v[64:67]
	v_mfma_f32_16x16x32_bf16 v[60:63], v[146:149], v[188:191], v[60:63]
	v_mfma_f32_16x16x32_bf16 v[56:59], v[154:157], v[188:191], v[56:59]
	v_mfma_f32_16x16x32_bf16 v[52:55], v[146:149], v[196:199], v[52:55]
	v_mfma_f32_16x16x32_bf16 v[48:51], v[154:157], v[196:199], v[48:51]
	v_mfma_f32_16x16x32_bf16 v[40:43], v[146:149], v[204:207], v[40:43]
	v_mfma_f32_16x16x32_bf16 v[32:35], v[154:157], v[204:207], v[32:35]
	v_mfma_f32_16x16x32_bf16 v[68:71], v[150:153], v[184:187], v[68:71]
	v_mfma_f32_16x16x32_bf16 v[64:67], v[172:175], v[184:187], v[64:67]
	v_mfma_f32_16x16x32_bf16 v[60:63], v[150:153], v[192:195], v[60:63]
	v_mfma_f32_16x16x32_bf16 v[56:59], v[172:175], v[192:195], v[56:59]
	v_mfma_f32_16x16x32_bf16 v[52:55], v[150:153], v[200:203], v[52:55]
	v_mfma_f32_16x16x32_bf16 v[48:51], v[172:175], v[200:203], v[48:51]
	v_mfma_f32_16x16x32_bf16 v[40:43], v[150:153], v[208:211], v[40:43]
	v_mfma_f32_16x16x32_bf16 v[32:35], v[172:175], v[208:211], v[32:35]
	s_setprio 0
	s_barrier
	s_add_i32 s50, s50, s61
	s_mov_b32 m0, s50
	ds_read_b128 v[180:183], v178 offset:16384
	ds_read_b128 v[184:187], v212 offset:16384
	ds_read_b128 v[188:191], v178 offset:18432
	ds_read_b128 v[192:195], v212 offset:18432
	ds_read_b128 v[196:199], v178 offset:20480
	ds_read_b128 v[200:203], v212 offset:20480
	ds_read_b128 v[204:207], v178 offset:22528
	ds_read_b128 v[208:211], v212 offset:22528
	s_nop 0
	global_load_lds_dwordx4 v168, s[34:35]
	s_add_i32 m0, s50, 0x2000
	s_add_u32 vcc_lo, s34, 0x8000
	s_addc_u32 vcc_hi, s35, 0
	s_add_i32 s50, s51, s61
	s_nop 0
	global_load_lds_dwordx4 v162, s[34:35]
	s_mov_b32 m0, s50
	s_nop 0
	global_load_lds_dwordx4 v168, vcc
	s_add_i32 m0, s50, 0x2000
	s_nop 0
	global_load_lds_dwordx4 v162, vcc
	s_waitcnt vmcnt(6)
	s_waitcnt lgkmcnt(0)
	s_barrier
	s_setprio 1
	s_waitcnt lgkmcnt(0)
	v_mfma_f32_16x16x32_bf16 v[44:47], v[130:133], v[180:183], v[44:47]
	v_mfma_f32_16x16x32_bf16 v[36:39], v[138:141], v[180:183], v[36:39]
	v_mfma_f32_16x16x32_bf16 v[28:31], v[130:133], v[188:191], v[28:31]
	v_mfma_f32_16x16x32_bf16 v[24:27], v[138:141], v[188:191], v[24:27]
	v_mfma_f32_16x16x32_bf16 v[20:23], v[130:133], v[196:199], v[20:23]
	v_mfma_f32_16x16x32_bf16 v[16:19], v[138:141], v[196:199], v[16:19]
	v_mfma_f32_16x16x32_bf16 v[12:15], v[130:133], v[204:207], v[12:15]
	v_mfma_f32_16x16x32_bf16 v[8:11], v[138:141], v[204:207], v[8:11]
	v_mfma_f32_16x16x32_bf16 v[44:47], v[134:137], v[184:187], v[44:47]
	v_mfma_f32_16x16x32_bf16 v[36:39], v[142:145], v[184:187], v[36:39]
	v_mfma_f32_16x16x32_bf16 v[28:31], v[134:137], v[192:195], v[28:31]
	v_mfma_f32_16x16x32_bf16 v[24:27], v[142:145], v[192:195], v[24:27]
	v_mfma_f32_16x16x32_bf16 v[20:23], v[134:137], v[200:203], v[20:23]
	v_mfma_f32_16x16x32_bf16 v[16:19], v[142:145], v[200:203], v[16:19]
	v_mfma_f32_16x16x32_bf16 v[12:15], v[134:137], v[208:211], v[12:15]
	v_mfma_f32_16x16x32_bf16 v[8:11], v[142:145], v[208:211], v[8:11]
	s_setprio 0
	s_setprio 1
	v_mfma_f32_16x16x32_bf16 v[4:7], v[146:149], v[180:183], v[4:7]
	v_mfma_f32_16x16x32_bf16 v[0:3], v[154:157], v[180:183], v[0:3]
	v_mfma_f32_16x16x32_bf16 v[104:107], v[146:149], v[188:191], v[104:107]
	v_mfma_f32_16x16x32_bf16 v[108:111], v[154:157], v[188:191], v[108:111]
	v_mfma_f32_16x16x32_bf16 v[112:115], v[146:149], v[196:199], v[112:115]
	v_mfma_f32_16x16x32_bf16 v[116:119], v[154:157], v[196:199], v[116:119]
	v_mfma_f32_16x16x32_bf16 v[120:123], v[146:149], v[204:207], v[120:123]
	v_mfma_f32_16x16x32_bf16 v[124:127], v[154:157], v[204:207], v[124:127]
	v_mfma_f32_16x16x32_bf16 v[4:7], v[150:153], v[184:187], v[4:7]
	v_mfma_f32_16x16x32_bf16 v[0:3], v[172:175], v[184:187], v[0:3]
	v_mfma_f32_16x16x32_bf16 v[104:107], v[150:153], v[192:195], v[104:107]
	v_mfma_f32_16x16x32_bf16 v[108:111], v[172:175], v[192:195], v[108:111]
	v_mfma_f32_16x16x32_bf16 v[112:115], v[150:153], v[200:203], v[112:115]
	v_mfma_f32_16x16x32_bf16 v[116:119], v[172:175], v[200:203], v[116:119]
	v_mfma_f32_16x16x32_bf16 v[120:123], v[150:153], v[208:211], v[120:123]
	v_mfma_f32_16x16x32_bf16 v[124:127], v[172:175], v[208:211], v[124:127]
	s_setprio 0
	s_barrier
	s_add_i32 s50, 0, 0x18000
	s_add_i32 s51, 0, 0x1c000
	v_add_u32_e32 v142, s50, v177
	v_add_u32_e32 v158, s51, v177
	ds_read_b128 v[130:133], v142
	ds_read_b128 v[134:137], v213 offset:32768
	ds_read_b128 v[138:141], v142 offset:2048
	ds_read_b128 v[142:145], v213 offset:34816
	ds_read_b128 v[146:149], v158
	ds_read_b128 v[150:153], v213 offset:49152
	ds_read_b128 v[154:157], v158 offset:2048
	ds_read_b128 v[172:175], v213 offset:51200
	s_mov_b32 m0, s29
	v_mov_b32_e32 v160, v129
	ds_read_b128 v[180:183], v178 offset:32768
	ds_read_b128 v[184:187], v212 offset:32768
	ds_read_b128 v[188:191], v178 offset:34816
	ds_read_b128 v[192:195], v212 offset:34816
	ds_read_b128 v[196:199], v178 offset:36864
	ds_read_b128 v[200:203], v212 offset:36864
	ds_read_b128 v[204:207], v178 offset:38912
	ds_read_b128 v[208:211], v212 offset:38912
	s_mov_b32 m0, s97
	s_nop 0
	global_load_lds_dwordx4 v164, s[24:25]
	s_mov_b32 m0, s28
	s_nop 0
	global_load_lds_dwordx4 v166, s[24:25]
	s_mov_b32 m0, s29
	v_mov_b32_e32 v170, v128
	global_load_lds_dwordx4 v160, s[24:25]
	s_mov_b32 m0, s30
	s_nop 0
	global_load_lds_dwordx4 v170, s[24:25]
	s_waitcnt vmcnt(8)
	s_waitcnt lgkmcnt(0)
	s_barrier
	s_setprio 1
	s_waitcnt lgkmcnt(0)
	v_mfma_f32_16x16x32_bf16 v[100:103], v[130:133], v[180:183], v[100:103]
	v_mfma_f32_16x16x32_bf16 v[96:99], v[138:141], v[180:183], v[96:99]
	v_mfma_f32_16x16x32_bf16 v[92:95], v[130:133], v[188:191], v[92:95]
	v_mfma_f32_16x16x32_bf16 v[88:91], v[138:141], v[188:191], v[88:91]
	v_mfma_f32_16x16x32_bf16 v[84:87], v[130:133], v[196:199], v[84:87]
	v_mfma_f32_16x16x32_bf16 v[80:83], v[138:141], v[196:199], v[80:83]
	v_mfma_f32_16x16x32_bf16 v[76:79], v[130:133], v[204:207], v[76:79]
	v_mfma_f32_16x16x32_bf16 v[72:75], v[138:141], v[204:207], v[72:75]
	v_mfma_f32_16x16x32_bf16 v[100:103], v[134:137], v[184:187], v[100:103]
	v_mfma_f32_16x16x32_bf16 v[96:99], v[142:145], v[184:187], v[96:99]
	v_mfma_f32_16x16x32_bf16 v[92:95], v[134:137], v[192:195], v[92:95]
	v_mfma_f32_16x16x32_bf16 v[88:91], v[142:145], v[192:195], v[88:91]
	v_mfma_f32_16x16x32_bf16 v[84:87], v[134:137], v[200:203], v[84:87]
	v_mfma_f32_16x16x32_bf16 v[80:83], v[142:145], v[200:203], v[80:83]
	v_mfma_f32_16x16x32_bf16 v[76:79], v[134:137], v[208:211], v[76:79]
	v_mfma_f32_16x16x32_bf16 v[72:75], v[142:145], v[208:211], v[72:75]
	s_setprio 0
	s_setprio 1
	v_mfma_f32_16x16x32_bf16 v[68:71], v[146:149], v[180:183], v[68:71]
	v_mfma_f32_16x16x32_bf16 v[64:67], v[154:157], v[180:183], v[64:67]
	v_mfma_f32_16x16x32_bf16 v[60:63], v[146:149], v[188:191], v[60:63]
	v_mfma_f32_16x16x32_bf16 v[56:59], v[154:157], v[188:191], v[56:59]
	v_mfma_f32_16x16x32_bf16 v[52:55], v[146:149], v[196:199], v[52:55]
	v_mfma_f32_16x16x32_bf16 v[48:51], v[154:157], v[196:199], v[48:51]
	v_mfma_f32_16x16x32_bf16 v[40:43], v[146:149], v[204:207], v[40:43]
	v_mfma_f32_16x16x32_bf16 v[32:35], v[154:157], v[204:207], v[32:35]
	v_mfma_f32_16x16x32_bf16 v[68:71], v[150:153], v[184:187], v[68:71]
	v_mfma_f32_16x16x32_bf16 v[64:67], v[172:175], v[184:187], v[64:67]
	v_mfma_f32_16x16x32_bf16 v[60:63], v[150:153], v[192:195], v[60:63]
	v_mfma_f32_16x16x32_bf16 v[56:59], v[172:175], v[192:195], v[56:59]
	v_mfma_f32_16x16x32_bf16 v[52:55], v[150:153], v[200:203], v[52:55]
	v_mfma_f32_16x16x32_bf16 v[48:51], v[172:175], v[200:203], v[48:51]
	v_mfma_f32_16x16x32_bf16 v[40:43], v[150:153], v[208:211], v[40:43]
	v_mfma_f32_16x16x32_bf16 v[32:35], v[172:175], v[208:211], v[32:35]
	s_setprio 0
	s_barrier
	v_mov_b32_e32 v169, v161
	ds_read_b128 v[180:183], v178 offset:49152
	ds_read_b128 v[184:187], v212 offset:49152
	ds_read_b128 v[188:191], v178 offset:51200
	ds_read_b128 v[192:195], v212 offset:51200
	ds_read_b128 v[196:199], v178 offset:53248
	ds_read_b128 v[200:203], v212 offset:53248
	ds_read_b128 v[204:207], v178 offset:55296
	ds_read_b128 v[208:211], v212 offset:55296
	s_add_i32 s50, s50, s61
	s_add_u32 vcc_lo, s34, s52
	s_addc_u32 vcc_hi, s35, s53
	s_mov_b32 m0, s50
	v_mov_b32_e32 v163, v161
	global_load_lds_dwordx4 v168, vcc
	s_add_i32 m0, s50, 0x2000
	v_mov_b32_e32 v165, v161
	s_add_u32 s34, s34, 0x8080
	s_addc_u32 s35, s35, 0
	s_add_i32 s50, s51, s61
	global_load_lds_dwordx4 v162, vcc
	s_mov_b32 m0, s50
	v_mov_b32_e32 v167, v161
	global_load_lds_dwordx4 v168, s[34:35]
	s_add_i32 m0, s50, 0x2000
	s_nop 0
	global_load_lds_dwordx4 v162, s[34:35]
	s_mov_b32 m0, s31
	s_add_u32 vcc_lo, s24, s52
	s_addc_u32 vcc_hi, s25, s53
	global_load_lds_dwordx4 v164, vcc
	s_mov_b32 m0, s42
	s_nop 0
	global_load_lds_dwordx4 v166, vcc
	s_waitcnt vmcnt(8)
	s_waitcnt lgkmcnt(0)
	s_barrier
	s_setprio 1
	s_waitcnt lgkmcnt(0)
	v_mfma_f32_16x16x32_bf16 v[44:47], v[130:133], v[180:183], v[44:47]
	v_mfma_f32_16x16x32_bf16 v[36:39], v[138:141], v[180:183], v[36:39]
	v_mfma_f32_16x16x32_bf16 v[28:31], v[130:133], v[188:191], v[28:31]
	v_mfma_f32_16x16x32_bf16 v[24:27], v[138:141], v[188:191], v[24:27]
	v_mfma_f32_16x16x32_bf16 v[20:23], v[130:133], v[196:199], v[20:23]
	v_mfma_f32_16x16x32_bf16 v[16:19], v[138:141], v[196:199], v[16:19]
	v_mfma_f32_16x16x32_bf16 v[12:15], v[130:133], v[204:207], v[12:15]
	v_mfma_f32_16x16x32_bf16 v[8:11], v[138:141], v[204:207], v[8:11]
	v_mfma_f32_16x16x32_bf16 v[44:47], v[134:137], v[184:187], v[44:47]
	v_mfma_f32_16x16x32_bf16 v[36:39], v[142:145], v[184:187], v[36:39]
	v_mfma_f32_16x16x32_bf16 v[28:31], v[134:137], v[192:195], v[28:31]
	v_mfma_f32_16x16x32_bf16 v[24:27], v[142:145], v[192:195], v[24:27]
	v_mfma_f32_16x16x32_bf16 v[20:23], v[134:137], v[200:203], v[20:23]
	v_mfma_f32_16x16x32_bf16 v[16:19], v[142:145], v[200:203], v[16:19]
	v_mfma_f32_16x16x32_bf16 v[12:15], v[134:137], v[208:211], v[12:15]
	v_mfma_f32_16x16x32_bf16 v[8:11], v[142:145], v[208:211], v[8:11]
	s_setprio 0
	s_setprio 1
	v_mfma_f32_16x16x32_bf16 v[4:7], v[146:149], v[180:183], v[4:7]
	v_mfma_f32_16x16x32_bf16 v[0:3], v[154:157], v[180:183], v[0:3]
	v_mfma_f32_16x16x32_bf16 v[104:107], v[146:149], v[188:191], v[104:107]
	v_mfma_f32_16x16x32_bf16 v[108:111], v[154:157], v[188:191], v[108:111]
	v_mfma_f32_16x16x32_bf16 v[112:115], v[146:149], v[196:199], v[112:115]
	v_mfma_f32_16x16x32_bf16 v[116:119], v[154:157], v[196:199], v[116:119]
	v_mfma_f32_16x16x32_bf16 v[120:123], v[146:149], v[204:207], v[120:123]
	v_mfma_f32_16x16x32_bf16 v[124:127], v[154:157], v[204:207], v[124:127]
	v_mfma_f32_16x16x32_bf16 v[4:7], v[150:153], v[184:187], v[4:7]
	v_mfma_f32_16x16x32_bf16 v[0:3], v[172:175], v[184:187], v[0:3]
	v_mfma_f32_16x16x32_bf16 v[104:107], v[150:153], v[192:195], v[104:107]
	v_mfma_f32_16x16x32_bf16 v[108:111], v[172:175], v[192:195], v[108:111]
	v_mfma_f32_16x16x32_bf16 v[112:115], v[150:153], v[200:203], v[112:115]
	v_mfma_f32_16x16x32_bf16 v[116:119], v[172:175], v[200:203], v[116:119]
	v_mfma_f32_16x16x32_bf16 v[120:123], v[150:153], v[208:211], v[120:123]
	v_mfma_f32_16x16x32_bf16 v[124:127], v[172:175], v[208:211], v[124:127]
	s_setprio 0
	s_barrier
	s_add_i32 s80, s80, 2
	s_add_u32 s6, s6, 0x100
	s_addc_u32 s7, s7, 0
	s_cmp_gt_u32 s80, 29
	s_cbranch_scc1 .LBB0_247

.LBB0_637:
	s_add_u32 s64, s6, s36
	v_add_u32_e32 v142, s53, v175
	v_add_u32_e32 v154, s54, v175
	s_addc_u32 s65, s7, s37
	ds_read_b128 v[130:133], v142
	ds_read_b128 v[138:141], v142 offset:2048
	v_xor_b32_e32 v142, 64, v142
	ds_read_b128 v[134:137], v142
	ds_read_b128 v[142:145], v142 offset:2048
	ds_read_b128 v[146:149], v154
	ds_read_b128 v[168:171], v154 offset:2048
	v_xor_b32_e32 v154, 64, v154
	ds_read_b128 v[150:153], v154
	ds_read_b128 v[178:181], v154 offset:2048
	s_add_u32 s66, s64, 0x46000100
	s_addc_u32 s67, s65, 0
	s_and_b64 s[38:39], s[40:41], exec
	s_cselect_b32 s39, s13, s67
	s_cselect_b32 s38, s12, s66
	s_add_u32 s66, s27, s36
	s_addc_u32 s67, s59, s37
	s_and_b64 s[40:41], s[40:41], exec
	s_cselect_b32 s41, s31, s67
	s_cselect_b32 s40, s30, s66
	ds_read_b128 v[182:185], v176
	ds_read_b128 v[186:189], v177
	ds_read_b128 v[190:193], v176 offset:2048
	ds_read_b128 v[194:197], v177 offset:2048
	ds_read_b128 v[198:201], v176 offset:4096
	ds_read_b128 v[202:205], v177 offset:4096
	ds_read_b128 v[206:209], v176 offset:6144
	ds_read_b128 v[210:213], v177 offset:6144
	s_add_i32 m0, s11, 0xc000
	s_add_u32 vcc_lo, s64, s20
	s_addc_u32 vcc_hi, s65, s21
	v_mov_b32_e32 v167, v157
	global_load_lds_dwordx4 v156, vcc
	s_add_i32 m0, s11, 0xe000
	s_nop 0
	global_load_lds_dwordx4 v166, vcc
	s_waitcnt vmcnt(8)
	s_waitcnt lgkmcnt(0)
	s_barrier
	s_setprio 1
	s_waitcnt lgkmcnt(0)
	v_mfma_f32_16x16x32_bf16 v[100:103], v[130:133], v[182:185], v[100:103]
	v_mfma_f32_16x16x32_bf16 v[96:99], v[138:141], v[182:185], v[96:99]
	v_mfma_f32_16x16x32_bf16 v[92:95], v[130:133], v[190:193], v[92:95]
	v_mfma_f32_16x16x32_bf16 v[88:91], v[138:141], v[190:193], v[88:91]
	v_mfma_f32_16x16x32_bf16 v[84:87], v[130:133], v[198:201], v[84:87]
	v_mfma_f32_16x16x32_bf16 v[76:79], v[138:141], v[198:201], v[76:79]
	v_mfma_f32_16x16x32_bf16 v[68:71], v[130:133], v[206:209], v[68:71]
	v_mfma_f32_16x16x32_bf16 v[60:63], v[138:141], v[206:209], v[60:63]
	v_mfma_f32_16x16x32_bf16 v[100:103], v[134:137], v[186:189], v[100:103]
	v_mfma_f32_16x16x32_bf16 v[96:99], v[142:145], v[186:189], v[96:99]
	v_mfma_f32_16x16x32_bf16 v[92:95], v[134:137], v[194:197], v[92:95]
	v_mfma_f32_16x16x32_bf16 v[88:91], v[142:145], v[194:197], v[88:91]
	v_mfma_f32_16x16x32_bf16 v[84:87], v[134:137], v[202:205], v[84:87]
	v_mfma_f32_16x16x32_bf16 v[76:79], v[142:145], v[202:205], v[76:79]
	v_mfma_f32_16x16x32_bf16 v[68:71], v[134:137], v[210:213], v[68:71]
	v_mfma_f32_16x16x32_bf16 v[60:63], v[142:145], v[210:213], v[60:63]
	s_setprio 0
	s_setprio 1
	v_mfma_f32_16x16x32_bf16 v[52:55], v[146:149], v[182:185], v[52:55]
	v_mfma_f32_16x16x32_bf16 v[44:47], v[168:171], v[182:185], v[44:47]
	v_mfma_f32_16x16x32_bf16 v[36:39], v[146:149], v[190:193], v[36:39]
	v_mfma_f32_16x16x32_bf16 v[28:31], v[168:171], v[190:193], v[28:31]
	v_mfma_f32_16x16x32_bf16 v[20:23], v[146:149], v[198:201], v[20:23]
	v_mfma_f32_16x16x32_bf16 v[12:15], v[168:171], v[198:201], v[12:15]
	v_mfma_f32_16x16x32_bf16 v[8:11], v[146:149], v[206:209], v[8:11]
	v_mfma_f32_16x16x32_bf16 v[4:7], v[168:171], v[206:209], v[4:7]
	v_mfma_f32_16x16x32_bf16 v[52:55], v[150:153], v[186:189], v[52:55]
	v_mfma_f32_16x16x32_bf16 v[44:47], v[178:181], v[186:189], v[44:47]
	v_mfma_f32_16x16x32_bf16 v[36:39], v[150:153], v[194:197], v[36:39]
	v_mfma_f32_16x16x32_bf16 v[28:31], v[178:181], v[194:197], v[28:31]
	v_mfma_f32_16x16x32_bf16 v[20:23], v[150:153], v[202:205], v[20:23]
	v_mfma_f32_16x16x32_bf16 v[12:15], v[178:181], v[202:205], v[12:15]
	v_mfma_f32_16x16x32_bf16 v[8:11], v[150:153], v[210:213], v[8:11]
	v_mfma_f32_16x16x32_bf16 v[4:7], v[178:181], v[210:213], v[4:7]
	s_setprio 0
	s_barrier
	s_add_i32 s64, s53, s42
	s_mov_b32 m0, s64
	ds_read_b128 v[182:185], v176 offset:16384
	ds_read_b128 v[186:189], v177 offset:16384
	ds_read_b128 v[190:193], v176 offset:18432
	ds_read_b128 v[194:197], v177 offset:18432
	ds_read_b128 v[198:201], v176 offset:20480
	ds_read_b128 v[202:205], v177 offset:20480
	ds_read_b128 v[206:209], v176 offset:22528
	ds_read_b128 v[210:213], v177 offset:22528
	s_nop 0
	global_load_lds_dwordx4 v164, s[40:41]
	s_add_i32 m0, s64, 0x2000
	s_add_u32 s64, s40, 0x8000
	s_addc_u32 s65, s41, 0
	s_add_i32 s66, s54, s42
	s_nop 0
	global_load_lds_dwordx4 v158, s[40:41]
	s_mov_b32 m0, s66
	s_nop 0
	global_load_lds_dwordx4 v164, s[64:65]
	s_add_i32 m0, s66, 0x2000
	s_nop 0
	global_load_lds_dwordx4 v158, s[64:65]
	s_waitcnt vmcnt(6)
	s_waitcnt lgkmcnt(0)
	s_barrier
	s_setprio 1
	s_waitcnt lgkmcnt(0)
	v_mfma_f32_16x16x32_bf16 v[80:83], v[130:133], v[182:185], v[80:83]
	v_mfma_f32_16x16x32_bf16 v[72:75], v[138:141], v[182:185], v[72:75]
	v_mfma_f32_16x16x32_bf16 v[64:67], v[130:133], v[190:193], v[64:67]
	v_mfma_f32_16x16x32_bf16 v[56:59], v[138:141], v[190:193], v[56:59]
	v_mfma_f32_16x16x32_bf16 v[48:51], v[130:133], v[198:201], v[48:51]
	v_mfma_f32_16x16x32_bf16 v[40:43], v[138:141], v[198:201], v[40:43]
	v_mfma_f32_16x16x32_bf16 v[32:35], v[130:133], v[206:209], v[32:35]
	v_mfma_f32_16x16x32_bf16 v[24:27], v[138:141], v[206:209], v[24:27]
	v_mfma_f32_16x16x32_bf16 v[80:83], v[134:137], v[186:189], v[80:83]
	v_mfma_f32_16x16x32_bf16 v[72:75], v[142:145], v[186:189], v[72:75]
	v_mfma_f32_16x16x32_bf16 v[64:67], v[134:137], v[194:197], v[64:67]
	v_mfma_f32_16x16x32_bf16 v[56:59], v[142:145], v[194:197], v[56:59]
	v_mfma_f32_16x16x32_bf16 v[48:51], v[134:137], v[202:205], v[48:51]
	v_mfma_f32_16x16x32_bf16 v[40:43], v[142:145], v[202:205], v[40:43]
	v_mfma_f32_16x16x32_bf16 v[32:35], v[134:137], v[210:213], v[32:35]
	v_mfma_f32_16x16x32_bf16 v[24:27], v[142:145], v[210:213], v[24:27]
	s_setprio 0
	s_setprio 1
	v_mfma_f32_16x16x32_bf16 v[16:19], v[146:149], v[182:185], v[16:19]
	v_mfma_f32_16x16x32_bf16 v[0:3], v[168:171], v[182:185], v[0:3]
	v_mfma_f32_16x16x32_bf16 v[104:107], v[146:149], v[190:193], v[104:107]
	v_mfma_f32_16x16x32_bf16 v[108:111], v[168:171], v[190:193], v[108:111]
	v_mfma_f32_16x16x32_bf16 v[112:115], v[146:149], v[198:201], v[112:115]
	v_mfma_f32_16x16x32_bf16 v[116:119], v[168:171], v[198:201], v[116:119]
	v_mfma_f32_16x16x32_bf16 v[120:123], v[146:149], v[206:209], v[120:123]
	v_mfma_f32_16x16x32_bf16 v[124:127], v[168:171], v[206:209], v[124:127]
	v_mfma_f32_16x16x32_bf16 v[16:19], v[150:153], v[186:189], v[16:19]
	v_mfma_f32_16x16x32_bf16 v[0:3], v[178:181], v[186:189], v[0:3]
	v_mfma_f32_16x16x32_bf16 v[104:107], v[150:153], v[194:197], v[104:107]
	v_mfma_f32_16x16x32_bf16 v[108:111], v[178:181], v[194:197], v[108:111]
	v_mfma_f32_16x16x32_bf16 v[112:115], v[150:153], v[202:205], v[112:115]
	v_mfma_f32_16x16x32_bf16 v[116:119], v[178:181], v[202:205], v[116:119]
	v_mfma_f32_16x16x32_bf16 v[120:123], v[150:153], v[210:213], v[120:123]
	v_mfma_f32_16x16x32_bf16 v[124:127], v[178:181], v[210:213], v[124:127]
	s_setprio 0
	s_barrier
	s_add_i32 s64, 0, 0x18000
	s_add_i32 s65, 0, 0x1c000
	v_add_u32_e32 v142, s64, v175
	v_add_u32_e32 v154, s65, v175
	ds_read_b128 v[130:133], v142
	ds_read_b128 v[138:141], v142 offset:2048
	v_xor_b32_e32 v142, 64, v142
	ds_read_b128 v[134:137], v142
	ds_read_b128 v[142:145], v142 offset:2048
	ds_read_b128 v[146:149], v154
	ds_read_b128 v[168:171], v154 offset:2048
	v_xor_b32_e32 v154, 64, v154
	ds_read_b128 v[150:153], v154
	ds_read_b128 v[178:181], v154 offset:2048
	s_mov_b32 m0, s45
	v_mov_b32_e32 v156, v129
	ds_read_b128 v[182:185], v176 offset:32768
	ds_read_b128 v[186:189], v177 offset:32768
	ds_read_b128 v[190:193], v176 offset:34816
	ds_read_b128 v[194:197], v177 offset:34816
	ds_read_b128 v[198:201], v176 offset:36864
	ds_read_b128 v[202:205], v177 offset:36864
	ds_read_b128 v[206:209], v176 offset:38912
	ds_read_b128 v[210:213], v177 offset:38912
	s_mov_b32 m0, s11
	s_nop 0
	global_load_lds_dwordx4 v160, s[38:39]
	s_mov_b32 m0, s44
	s_nop 0
	global_load_lds_dwordx4 v162, s[38:39]
	s_mov_b32 m0, s45
	v_mov_b32_e32 v166, v128
	global_load_lds_dwordx4 v156, s[38:39]
	s_mov_b32 m0, s46
	s_nop 0
	global_load_lds_dwordx4 v166, s[38:39]
	s_waitcnt vmcnt(8)
	s_waitcnt lgkmcnt(0)
	s_barrier
	s_setprio 1
	s_waitcnt lgkmcnt(0)
	v_mfma_f32_16x16x32_bf16 v[100:103], v[130:133], v[182:185], v[100:103]
	v_mfma_f32_16x16x32_bf16 v[96:99], v[138:141], v[182:185], v[96:99]
	v_mfma_f32_16x16x32_bf16 v[92:95], v[130:133], v[190:193], v[92:95]
	v_mfma_f32_16x16x32_bf16 v[88:91], v[138:141], v[190:193], v[88:91]
	v_mfma_f32_16x16x32_bf16 v[84:87], v[130:133], v[198:201], v[84:87]
	v_mfma_f32_16x16x32_bf16 v[76:79], v[138:141], v[198:201], v[76:79]
	v_mfma_f32_16x16x32_bf16 v[68:71], v[130:133], v[206:209], v[68:71]
	v_mfma_f32_16x16x32_bf16 v[60:63], v[138:141], v[206:209], v[60:63]
	v_mfma_f32_16x16x32_bf16 v[100:103], v[134:137], v[186:189], v[100:103]
	v_mfma_f32_16x16x32_bf16 v[96:99], v[142:145], v[186:189], v[96:99]
	v_mfma_f32_16x16x32_bf16 v[92:95], v[134:137], v[194:197], v[92:95]
	v_mfma_f32_16x16x32_bf16 v[88:91], v[142:145], v[194:197], v[88:91]
	v_mfma_f32_16x16x32_bf16 v[84:87], v[134:137], v[202:205], v[84:87]
	v_mfma_f32_16x16x32_bf16 v[76:79], v[142:145], v[202:205], v[76:79]
	v_mfma_f32_16x16x32_bf16 v[68:71], v[134:137], v[210:213], v[68:71]
	v_mfma_f32_16x16x32_bf16 v[60:63], v[142:145], v[210:213], v[60:63]
	s_setprio 0
	s_setprio 1
	v_mfma_f32_16x16x32_bf16 v[52:55], v[146:149], v[182:185], v[52:55]
	v_mfma_f32_16x16x32_bf16 v[44:47], v[168:171], v[182:185], v[44:47]
	v_mfma_f32_16x16x32_bf16 v[36:39], v[146:149], v[190:193], v[36:39]
	v_mfma_f32_16x16x32_bf16 v[28:31], v[168:171], v[190:193], v[28:31]
	v_mfma_f32_16x16x32_bf16 v[20:23], v[146:149], v[198:201], v[20:23]
	v_mfma_f32_16x16x32_bf16 v[12:15], v[168:171], v[198:201], v[12:15]
	v_mfma_f32_16x16x32_bf16 v[8:11], v[146:149], v[206:209], v[8:11]
	v_mfma_f32_16x16x32_bf16 v[4:7], v[168:171], v[206:209], v[4:7]
	v_mfma_f32_16x16x32_bf16 v[52:55], v[150:153], v[186:189], v[52:55]
	v_mfma_f32_16x16x32_bf16 v[44:47], v[178:181], v[186:189], v[44:47]
	v_mfma_f32_16x16x32_bf16 v[36:39], v[150:153], v[194:197], v[36:39]
	v_mfma_f32_16x16x32_bf16 v[28:31], v[178:181], v[194:197], v[28:31]
	v_mfma_f32_16x16x32_bf16 v[20:23], v[150:153], v[202:205], v[20:23]
	v_mfma_f32_16x16x32_bf16 v[12:15], v[178:181], v[202:205], v[12:15]
	v_mfma_f32_16x16x32_bf16 v[8:11], v[150:153], v[210:213], v[8:11]
	v_mfma_f32_16x16x32_bf16 v[4:7], v[178:181], v[210:213], v[4:7]
	s_setprio 0
	s_barrier
	v_mov_b32_e32 v165, v157
	ds_read_b128 v[182:185], v176 offset:49152
	ds_read_b128 v[186:189], v177 offset:49152
	ds_read_b128 v[190:193], v176 offset:51200
	ds_read_b128 v[194:197], v177 offset:51200
	ds_read_b128 v[198:201], v176 offset:53248
	ds_read_b128 v[202:205], v177 offset:53248
	ds_read_b128 v[206:209], v176 offset:55296
	ds_read_b128 v[210:213], v177 offset:55296
	s_add_i32 s64, s64, s42
	s_add_u32 vcc_lo, s40, s18
	s_addc_u32 vcc_hi, s41, s19
	s_mov_b32 m0, s64
	v_mov_b32_e32 v159, v157
	global_load_lds_dwordx4 v164, vcc
	s_add_i32 m0, s64, 0x2000
	v_mov_b32_e32 v161, v157
	s_add_u32 s40, s40, 0x8080
	s_addc_u32 s41, s41, 0
	s_add_i32 s64, s65, s42
	global_load_lds_dwordx4 v158, vcc
	s_mov_b32 m0, s64
	v_mov_b32_e32 v163, v157
	global_load_lds_dwordx4 v164, s[40:41]
	s_add_i32 m0, s64, 0x2000
	s_nop 0
	global_load_lds_dwordx4 v158, s[40:41]
	s_mov_b32 m0, s49
	s_add_u32 vcc_lo, s38, s18
	s_addc_u32 vcc_hi, s39, s19
	global_load_lds_dwordx4 v160, vcc
	s_mov_b32 m0, s50
	s_nop 0
	global_load_lds_dwordx4 v162, vcc
	s_waitcnt vmcnt(8)
	s_waitcnt lgkmcnt(0)
	s_barrier
	s_setprio 1
	s_waitcnt lgkmcnt(0)
	v_mfma_f32_16x16x32_bf16 v[80:83], v[130:133], v[182:185], v[80:83]
	v_mfma_f32_16x16x32_bf16 v[72:75], v[138:141], v[182:185], v[72:75]
	v_mfma_f32_16x16x32_bf16 v[64:67], v[130:133], v[190:193], v[64:67]
	v_mfma_f32_16x16x32_bf16 v[56:59], v[138:141], v[190:193], v[56:59]
	v_mfma_f32_16x16x32_bf16 v[48:51], v[130:133], v[198:201], v[48:51]
	v_mfma_f32_16x16x32_bf16 v[40:43], v[138:141], v[198:201], v[40:43]
	v_mfma_f32_16x16x32_bf16 v[32:35], v[130:133], v[206:209], v[32:35]
	v_mfma_f32_16x16x32_bf16 v[24:27], v[138:141], v[206:209], v[24:27]
	v_mfma_f32_16x16x32_bf16 v[80:83], v[134:137], v[186:189], v[80:83]
	v_mfma_f32_16x16x32_bf16 v[72:75], v[142:145], v[186:189], v[72:75]
	v_mfma_f32_16x16x32_bf16 v[64:67], v[134:137], v[194:197], v[64:67]
	v_mfma_f32_16x16x32_bf16 v[56:59], v[142:145], v[194:197], v[56:59]
	v_mfma_f32_16x16x32_bf16 v[48:51], v[134:137], v[202:205], v[48:51]
	v_mfma_f32_16x16x32_bf16 v[40:43], v[142:145], v[202:205], v[40:43]
	v_mfma_f32_16x16x32_bf16 v[32:35], v[134:137], v[210:213], v[32:35]
	v_mfma_f32_16x16x32_bf16 v[24:27], v[142:145], v[210:213], v[24:27]
	s_setprio 0
	s_setprio 1
	v_mfma_f32_16x16x32_bf16 v[16:19], v[146:149], v[182:185], v[16:19]
	v_mfma_f32_16x16x32_bf16 v[0:3], v[168:171], v[182:185], v[0:3]
	v_mfma_f32_16x16x32_bf16 v[104:107], v[146:149], v[190:193], v[104:107]
	v_mfma_f32_16x16x32_bf16 v[108:111], v[168:171], v[190:193], v[108:111]
	v_mfma_f32_16x16x32_bf16 v[112:115], v[146:149], v[198:201], v[112:115]
	v_mfma_f32_16x16x32_bf16 v[116:119], v[168:171], v[198:201], v[116:119]
	v_mfma_f32_16x16x32_bf16 v[120:123], v[146:149], v[206:209], v[120:123]
	v_mfma_f32_16x16x32_bf16 v[124:127], v[168:171], v[206:209], v[124:127]
	v_mfma_f32_16x16x32_bf16 v[16:19], v[150:153], v[186:189], v[16:19]
	v_mfma_f32_16x16x32_bf16 v[0:3], v[178:181], v[186:189], v[0:3]
	v_mfma_f32_16x16x32_bf16 v[104:107], v[150:153], v[194:197], v[104:107]
	v_mfma_f32_16x16x32_bf16 v[108:111], v[178:181], v[194:197], v[108:111]
	v_mfma_f32_16x16x32_bf16 v[112:115], v[150:153], v[202:205], v[112:115]
	v_mfma_f32_16x16x32_bf16 v[116:119], v[178:181], v[202:205], v[116:119]
	v_mfma_f32_16x16x32_bf16 v[120:123], v[150:153], v[210:213], v[120:123]
	v_mfma_f32_16x16x32_bf16 v[124:127], v[178:181], v[210:213], v[124:127]
	s_setprio 0
	s_barrier
	s_add_i32 s63, s63, 2
	s_add_u32 s36, s36, 0x100
	s_addc_u32 s37, s37, 0
	s_cmp_gt_u32 s63, 29
	s_cbranch_scc1 .LBB0_642

.LBB0_910:
	s_add_u32 s25, s36, 0x100
	s_addc_u32 s27, s37, 0
	s_lshl_b32 s7, s55, 10
	s_add_i32 s7, s7, 0x24000
	s_mov_b32 s42, -2
	s_mov_b64 s[36:37], 0
	s_cmp_eq_u32 s42, 12
	s_cselect_b64 s[40:41], -1, 0
	s_and_b64 s[38:39], s[34:35], s[40:41]
	s_andn2_b64 vcc, exec, s[38:39]
	v_mov_b32_e32 v128, v186
	v_mov_b32_e32 v129, v176
	s_add_u32 s76, s10, s36
	v_add_u32_e32 v134, s67, v194
	v_add_u32_e32 v142, s67, v195
	v_add_u32_e32 v150, s68, v194
	v_add_u32_e32 v158, s68, v195
	s_addc_u32 s77, s11, s37
	ds_read_b128 v[130:133], v134
	ds_read_b128 v[138:141], v134 offset:2048
	ds_read_b128 v[134:137], v142
	ds_read_b128 v[142:145], v142 offset:2048
	ds_read_b128 v[146:149], v150
	ds_read_b128 v[154:157], v150 offset:2048
	ds_read_b128 v[150:153], v158
	ds_read_b128 v[158:161], v158 offset:2048
	s_add_u32 s43, s76, 0x36000100
	s_addc_u32 s75, s77, 0
	s_and_b64 s[38:39], s[40:41], exec
	s_cselect_b32 s39, s13, s75
	s_cselect_b32 s38, s12, s43
	s_add_u32 s43, s25, s36
	s_addc_u32 s75, s27, s37
	s_and_b64 s[40:41], s[40:41], exec
	s_cselect_b32 s41, s31, s75
	s_cselect_b32 s40, s30, s43
	ds_read_b128 v[162:165], v227
	ds_read_b128 v[232:235], v227 offset:2048
	ds_read_b128 v[166:169], v228
	ds_read_b128 v[236:239], v228 offset:2048
	ds_read_b128 v[240:243], v227 offset:4096
	ds_read_b128 v[196:199], v227 offset:6144
	ds_read_b128 v[244:247], v228 offset:4096
	ds_read_b128 v[200:203], v228 offset:6144
	s_add_i32 m0, s50, 0xc000
	s_add_u32 vcc_lo, s76, s16
	s_addc_u32 vcc_hi, s77, s17
	v_mov_b32_e32 v187, v177
	global_load_lds_dwordx4 v176, vcc
	s_add_i32 m0, s50, 0xe000
	s_nop 0
	global_load_lds_dwordx4 v186, vcc
	s_waitcnt vmcnt(8)
	s_waitcnt lgkmcnt(0)
	s_barrier
	s_setprio 1
	s_waitcnt lgkmcnt(0)
	v_mfma_f32_16x16x128_f8f6f4 v[100:103], v[130:137], v[162:169], 0
	v_mfma_f32_16x16x128_f8f6f4 v[96:99], v[138:145], v[162:169], 0
	v_mfma_f32_16x16x128_f8f6f4 v[92:95], v[130:137], v[232:239], 0
	v_mfma_f32_16x16x128_f8f6f4 v[88:91], v[138:145], v[232:239], 0
	v_mfma_f32_16x16x128_f8f6f4 v[84:87], v[130:137], v[240:247], 0
	v_mfma_f32_16x16x128_f8f6f4 v[80:83], v[138:145], v[240:247], 0
	v_mfma_f32_16x16x128_f8f6f4 v[170:173], v[130:137], v[196:203], 0
	v_mfma_f32_16x16x128_f8f6f4 v[188:191], v[138:145], v[196:203], 0
	s_setprio 0
	s_setprio 1
	v_mfma_f32_16x16x128_f8f6f4 v[40:43], v[146:153], v[196:203], 0
	v_mfma_f32_16x16x128_f8f6f4 v[32:35], v[154:161], v[196:203], 0
	v_mfma_f32_16x16x128_f8f6f4 v[248:251], v[146:153], v[162:169], 0
	v_mfma_f32_16x16x128_f8f6f4 v[204:207], v[154:161], v[162:169], 0
	v_mfma_f32_16x16x128_f8f6f4 v[208:211], v[146:153], v[232:239], 0
	v_mfma_f32_16x16x128_f8f6f4 v[212:215], v[154:161], v[232:239], 0
	v_mfma_f32_16x16x128_f8f6f4 v[216:219], v[146:153], v[240:247], 0
	v_mfma_f32_16x16x128_f8f6f4 v[240:243], v[154:161], v[240:247], 0
	s_setprio 0
	s_barrier
	s_add_i32 s43, s67, s5
	s_mov_b32 m0, s43
	s_nop 2
	ds_read_b128 v[48:51], v227 offset:16384
	ds_read_b128 v[56:59], v227 offset:18432
	ds_read_b128 v[52:55], v228 offset:16384
	ds_read_b128 v[60:63], v228 offset:18432
	ds_read_b128 v[64:67], v227 offset:20480
	ds_read_b128 v[72:75], v227 offset:22528
	ds_read_b128 v[68:71], v228 offset:20480
	ds_read_b128 v[76:79], v228 offset:22528
	s_nop 0
	global_load_lds_dwordx4 v184, s[40:41]
	s_add_i32 m0, s43, 0x2000
	s_add_u32 s76, s40, 0x4000
	s_addc_u32 s77, s41, 0
	s_add_i32 s43, s68, s5
	s_nop 0
	global_load_lds_dwordx4 v178, s[40:41]
	s_mov_b32 m0, s43
	s_nop 0
	global_load_lds_dwordx4 v184, s[76:77]
	s_add_i32 m0, s43, 0x2000
	s_nop 0
	global_load_lds_dwordx4 v178, s[76:77]
	s_waitcnt vmcnt(6)
	s_waitcnt lgkmcnt(0)
	s_barrier
	s_setprio 1
	s_waitcnt lgkmcnt(0)
	v_mfma_f32_16x16x128_f8f6f4 v[44:47], v[130:137], v[48:55], 0
	v_mfma_f32_16x16x128_f8f6f4 v[36:39], v[138:145], v[48:55], 0
	v_mfma_f32_16x16x128_f8f6f4 v[28:31], v[130:137], v[56:63], 0
	v_mfma_f32_16x16x128_f8f6f4 v[24:27], v[138:145], v[56:63], 0
	v_mfma_f32_16x16x128_f8f6f4 v[20:23], v[130:137], v[64:71], 0
	v_mfma_f32_16x16x128_f8f6f4 v[16:19], v[138:145], v[64:71], 0
	v_mfma_f32_16x16x128_f8f6f4 v[12:15], v[130:137], v[72:79], 0
	v_mfma_f32_16x16x128_f8f6f4 v[8:11], v[138:145], v[72:79], 0
	s_setprio 0
	s_setprio 1
	v_mfma_f32_16x16x128_f8f6f4 v[4:7], v[146:153], v[48:55], 0
	v_mfma_f32_16x16x128_f8f6f4 v[0:3], v[154:161], v[48:55], 0
	v_mfma_f32_16x16x128_f8f6f4 v[104:107], v[146:153], v[56:63], 0
	v_mfma_f32_16x16x128_f8f6f4 v[108:111], v[154:161], v[56:63], 0
	v_mfma_f32_16x16x128_f8f6f4 v[112:115], v[146:153], v[64:71], 0
	v_mfma_f32_16x16x128_f8f6f4 v[116:119], v[154:161], v[64:71], 0
	v_mfma_f32_16x16x128_f8f6f4 v[120:123], v[146:153], v[72:79], 0
	v_mfma_f32_16x16x128_f8f6f4 v[124:127], v[154:161], v[72:79], 0
	s_setprio 0
	s_barrier
	s_add_i32 s43, 0, 0x18000
	v_add_u32_e32 v48, s43, v194
	s_add_i32 s75, 0, 0x1c000
	v_add_u32_e32 v49, s43, v195
	ds_read_b128 v[130:133], v48
	ds_read_b128 v[138:141], v48 offset:2048
	ds_read_b128 v[134:137], v49
	ds_read_b128 v[142:145], v49 offset:2048
	v_add_u32_e32 v48, s75, v194
	v_add_u32_e32 v49, s75, v195
	ds_read_b128 v[146:149], v48
	ds_read_b128 v[154:157], v48 offset:2048
	ds_read_b128 v[150:153], v49
	ds_read_b128 v[158:161], v49 offset:2048
	s_mov_b32 m0, s52
	v_mov_b32_e32 v176, v129
	ds_read_b128 v[48:51], v227 offset:32768
	ds_read_b128 v[162:165], v227 offset:34816
	ds_read_b128 v[52:55], v228 offset:32768
	ds_read_b128 v[166:169], v228 offset:34816
	ds_read_b128 v[196:199], v227 offset:36864
	ds_read_b128 v[232:235], v227 offset:38912
	ds_read_b128 v[200:203], v228 offset:36864
	ds_read_b128 v[236:239], v228 offset:38912
	s_mov_b32 m0, s50
	s_nop 0
	global_load_lds_dwordx4 v180, s[38:39]
	s_mov_b32 m0, s51
	s_nop 0
	global_load_lds_dwordx4 v182, s[38:39]
	s_mov_b32 m0, s52
	v_mov_b32_e32 v186, v128
	global_load_lds_dwordx4 v176, s[38:39]
	s_mov_b32 m0, s53
	s_nop 0
	global_load_lds_dwordx4 v186, s[38:39]
	s_waitcnt vmcnt(8)
	s_waitcnt lgkmcnt(0)
	s_barrier
	s_setprio 1
	s_waitcnt lgkmcnt(0)
	v_mfma_f32_16x16x128_f8f6f4 v[100:103], v[130:137], v[48:55], v[100:103]
	v_mfma_f32_16x16x128_f8f6f4 v[96:99], v[138:145], v[48:55], v[96:99]
	v_mfma_f32_16x16x128_f8f6f4 v[92:95], v[130:137], v[162:169], v[92:95]
	v_mfma_f32_16x16x128_f8f6f4 v[88:91], v[138:145], v[162:169], v[88:91]
	v_mfma_f32_16x16x128_f8f6f4 v[84:87], v[130:137], v[196:203], v[84:87]
	v_mfma_f32_16x16x128_f8f6f4 v[80:83], v[138:145], v[196:203], v[80:83]
	v_mfma_f32_16x16x128_f8f6f4 v[76:79], v[130:137], v[232:239], v[170:173]
	v_mfma_f32_16x16x128_f8f6f4 v[72:75], v[138:145], v[232:239], v[188:191]
	s_setprio 0
	s_setprio 1
	v_mfma_f32_16x16x128_f8f6f4 v[68:71], v[146:153], v[48:55], v[248:251]
	v_mfma_f32_16x16x128_f8f6f4 v[64:67], v[154:161], v[48:55], v[204:207]
	v_mfma_f32_16x16x128_f8f6f4 v[60:63], v[146:153], v[162:169], v[208:211]
	v_mfma_f32_16x16x128_f8f6f4 v[56:59], v[154:161], v[162:169], v[212:215]
	v_mfma_f32_16x16x128_f8f6f4 v[52:55], v[146:153], v[196:203], v[216:219]
	v_mfma_f32_16x16x128_f8f6f4 v[48:51], v[154:161], v[196:203], v[240:243]
	v_mfma_f32_16x16x128_f8f6f4 v[40:43], v[146:153], v[232:239], v[40:43]
	v_mfma_f32_16x16x128_f8f6f4 v[32:35], v[154:161], v[232:239], v[32:35]
	s_setprio 0
	s_barrier
	v_mov_b32_e32 v185, v177
	ds_read_b128 v[162:165], v227 offset:49152
	ds_read_b128 v[196:199], v227 offset:51200
	ds_read_b128 v[166:169], v228 offset:49152
	ds_read_b128 v[200:203], v228 offset:51200
	ds_read_b128 v[232:235], v227 offset:53248
	ds_read_b128 v[240:243], v227 offset:55296
	ds_read_b128 v[236:239], v228 offset:53248
	ds_read_b128 v[244:247], v228 offset:55296
	s_add_i32 s43, s43, s5
	s_add_u32 vcc_lo, s40, s14
	s_addc_u32 vcc_hi, s41, s15
	s_mov_b32 m0, s43
	v_mov_b32_e32 v179, v177
	global_load_lds_dwordx4 v184, vcc
	s_add_i32 m0, s43, 0x2000
	v_mov_b32_e32 v181, v177
	s_add_u32 s40, s40, 0x4080
	s_addc_u32 s41, s41, 0
	s_add_i32 s43, s75, s5
	global_load_lds_dwordx4 v178, vcc
	s_mov_b32 m0, s43
	v_mov_b32_e32 v183, v177
	global_load_lds_dwordx4 v184, s[40:41]
	s_add_i32 m0, s43, 0x2000
	s_nop 0
	global_load_lds_dwordx4 v178, s[40:41]
	s_mov_b32 m0, s62
	s_add_u32 vcc_lo, s38, s14
	s_addc_u32 vcc_hi, s39, s15
	global_load_lds_dwordx4 v180, vcc
	s_mov_b32 m0, s63
	s_nop 0
	global_load_lds_dwordx4 v182, vcc
	s_waitcnt vmcnt(8)
	s_waitcnt lgkmcnt(0)
	s_barrier
	s_setprio 1
	s_waitcnt lgkmcnt(0)
	v_mfma_f32_16x16x128_f8f6f4 v[44:47], v[130:137], v[162:169], v[44:47]
	v_mfma_f32_16x16x128_f8f6f4 v[36:39], v[138:145], v[162:169], v[36:39]
	v_mfma_f32_16x16x128_f8f6f4 v[28:31], v[130:137], v[196:203], v[28:31]
	v_mfma_f32_16x16x128_f8f6f4 v[24:27], v[138:145], v[196:203], v[24:27]
	v_mfma_f32_16x16x128_f8f6f4 v[20:23], v[130:137], v[232:239], v[20:23]
	v_mfma_f32_16x16x128_f8f6f4 v[16:19], v[138:145], v[232:239], v[16:19]
	v_mfma_f32_16x16x128_f8f6f4 v[12:15], v[130:137], v[240:247], v[12:15]
	v_mfma_f32_16x16x128_f8f6f4 v[8:11], v[138:145], v[240:247], v[8:11]
	s_setprio 0
	s_setprio 1
	v_mfma_f32_16x16x128_f8f6f4 v[4:7], v[146:153], v[162:169], v[4:7]
	v_mfma_f32_16x16x128_f8f6f4 v[0:3], v[154:161], v[162:169], v[0:3]
	v_mfma_f32_16x16x128_f8f6f4 v[104:107], v[146:153], v[196:203], v[104:107]
	v_mfma_f32_16x16x128_f8f6f4 v[108:111], v[154:161], v[196:203], v[108:111]
	v_mfma_f32_16x16x128_f8f6f4 v[112:115], v[146:153], v[232:239], v[112:115]
	v_mfma_f32_16x16x128_f8f6f4 v[116:119], v[154:161], v[232:239], v[116:119]
	v_mfma_f32_16x16x128_f8f6f4 v[120:123], v[146:153], v[240:247], v[120:123]
	v_mfma_f32_16x16x128_f8f6f4 v[124:127], v[154:161], v[240:247], v[124:127]
	s_setprio 0
	s_barrier
	s_add_i32 s42, s42, 2
	s_add_u32 s36, s36, 0x100
	s_addc_u32 s37, s37, 0
	s_branch .LBB0_912
.LBB0_911:
	s_add_u32 s76, s10, s36
	v_add_u32_e32 v134, s67, v194
	v_add_u32_e32 v142, s67, v195
	v_add_u32_e32 v150, s68, v194
	v_add_u32_e32 v158, s68, v195
	s_addc_u32 s77, s11, s37
	ds_read_b128 v[130:133], v134
	ds_read_b128 v[138:141], v134 offset:2048
	ds_read_b128 v[134:137], v142
	ds_read_b128 v[142:145], v142 offset:2048
	ds_read_b128 v[146:149], v150
	ds_read_b128 v[154:157], v150 offset:2048
	ds_read_b128 v[150:153], v158
	ds_read_b128 v[158:161], v158 offset:2048
	s_add_u32 s43, s76, 0x36000100
	s_addc_u32 s75, s77, 0
	s_and_b64 s[38:39], s[40:41], exec
	s_cselect_b32 s39, s13, s75
	s_cselect_b32 s38, s12, s43
	s_add_u32 s43, s25, s36
	s_addc_u32 s75, s27, s37
	s_and_b64 s[40:41], s[40:41], exec
	s_cselect_b32 s41, s31, s75
	s_cselect_b32 s40, s30, s43
	ds_read_b128 v[162:165], v227
	ds_read_b128 v[232:235], v227 offset:2048
	ds_read_b128 v[166:169], v228
	ds_read_b128 v[236:239], v228 offset:2048
	ds_read_b128 v[240:243], v227 offset:4096
	ds_read_b128 v[196:199], v227 offset:6144
	ds_read_b128 v[244:247], v228 offset:4096
	ds_read_b128 v[200:203], v228 offset:6144
	s_add_i32 m0, s50, 0xc000
	s_add_u32 vcc_lo, s76, s16
	s_addc_u32 vcc_hi, s77, s17
	v_mov_b32_e32 v187, v177
	global_load_lds_dwordx4 v176, vcc
	s_add_i32 m0, s50, 0xe000
	s_nop 0
	global_load_lds_dwordx4 v186, vcc
	s_waitcnt vmcnt(8)
	s_waitcnt lgkmcnt(0)
	s_barrier
	s_setprio 1
	s_waitcnt lgkmcnt(0)
	v_mfma_f32_16x16x128_f8f6f4 v[100:103], v[130:137], v[162:169], v[100:103]
	v_mfma_f32_16x16x128_f8f6f4 v[96:99], v[138:145], v[162:169], v[96:99]
	v_mfma_f32_16x16x128_f8f6f4 v[92:95], v[130:137], v[232:239], v[92:95]
	v_mfma_f32_16x16x128_f8f6f4 v[88:91], v[138:145], v[232:239], v[88:91]
	v_mfma_f32_16x16x128_f8f6f4 v[84:87], v[130:137], v[240:247], v[84:87]
	v_mfma_f32_16x16x128_f8f6f4 v[80:83], v[138:145], v[240:247], v[80:83]
	v_mfma_f32_16x16x128_f8f6f4 v[170:173], v[130:137], v[196:203], v[76:79]
	v_mfma_f32_16x16x128_f8f6f4 v[188:191], v[138:145], v[196:203], v[72:75]
	s_setprio 0
	s_setprio 1
	v_mfma_f32_16x16x128_f8f6f4 v[40:43], v[146:153], v[196:203], v[40:43]
	v_mfma_f32_16x16x128_f8f6f4 v[32:35], v[154:161], v[196:203], v[32:35]
	v_mfma_f32_16x16x128_f8f6f4 v[248:251], v[146:153], v[162:169], v[68:71]
	v_mfma_f32_16x16x128_f8f6f4 v[204:207], v[154:161], v[162:169], v[64:67]
	v_mfma_f32_16x16x128_f8f6f4 v[208:211], v[146:153], v[232:239], v[60:63]
	v_mfma_f32_16x16x128_f8f6f4 v[212:215], v[154:161], v[232:239], v[56:59]
	v_mfma_f32_16x16x128_f8f6f4 v[216:219], v[146:153], v[240:247], v[52:55]
	v_mfma_f32_16x16x128_f8f6f4 v[240:243], v[154:161], v[240:247], v[48:51]
	s_setprio 0
	s_barrier
	s_add_i32 s43, s67, s5
	s_mov_b32 m0, s43
	s_nop 2
	ds_read_b128 v[48:51], v227 offset:16384
	ds_read_b128 v[56:59], v227 offset:18432
	ds_read_b128 v[52:55], v228 offset:16384
	ds_read_b128 v[60:63], v228 offset:18432
	ds_read_b128 v[64:67], v227 offset:20480
	ds_read_b128 v[72:75], v227 offset:22528
	ds_read_b128 v[68:71], v228 offset:20480
	ds_read_b128 v[76:79], v228 offset:22528
	s_nop 0
	global_load_lds_dwordx4 v184, s[40:41]
	s_add_i32 m0, s43, 0x2000
	s_add_u32 s76, s40, 0x4000
	s_addc_u32 s77, s41, 0
	s_add_i32 s43, s68, s5
	s_nop 0
	global_load_lds_dwordx4 v178, s[40:41]
	s_mov_b32 m0, s43
	s_nop 0
	global_load_lds_dwordx4 v184, s[76:77]
	s_add_i32 m0, s43, 0x2000
	s_nop 0
	global_load_lds_dwordx4 v178, s[76:77]
	s_waitcnt vmcnt(6)
	s_waitcnt lgkmcnt(0)
	s_barrier
	s_setprio 1
	s_waitcnt lgkmcnt(0)
	v_mfma_f32_16x16x128_f8f6f4 v[44:47], v[130:137], v[48:55], v[44:47]
	v_mfma_f32_16x16x128_f8f6f4 v[36:39], v[138:145], v[48:55], v[36:39]
	v_mfma_f32_16x16x128_f8f6f4 v[28:31], v[130:137], v[56:63], v[28:31]
	v_mfma_f32_16x16x128_f8f6f4 v[24:27], v[138:145], v[56:63], v[24:27]
	v_mfma_f32_16x16x128_f8f6f4 v[20:23], v[130:137], v[64:71], v[20:23]
	v_mfma_f32_16x16x128_f8f6f4 v[16:19], v[138:145], v[64:71], v[16:19]
	v_mfma_f32_16x16x128_f8f6f4 v[12:15], v[130:137], v[72:79], v[12:15]
	v_mfma_f32_16x16x128_f8f6f4 v[8:11], v[138:145], v[72:79], v[8:11]
	s_setprio 0
	s_setprio 1
	v_mfma_f32_16x16x128_f8f6f4 v[4:7], v[146:153], v[48:55], v[4:7]
	v_mfma_f32_16x16x128_f8f6f4 v[0:3], v[154:161], v[48:55], v[0:3]
	v_mfma_f32_16x16x128_f8f6f4 v[104:107], v[146:153], v[56:63], v[104:107]
	v_mfma_f32_16x16x128_f8f6f4 v[108:111], v[154:161], v[56:63], v[108:111]
	v_mfma_f32_16x16x128_f8f6f4 v[112:115], v[146:153], v[64:71], v[112:115]
	v_mfma_f32_16x16x128_f8f6f4 v[116:119], v[154:161], v[64:71], v[116:119]
	v_mfma_f32_16x16x128_f8f6f4 v[120:123], v[146:153], v[72:79], v[120:123]
	v_mfma_f32_16x16x128_f8f6f4 v[124:127], v[154:161], v[72:79], v[124:127]
	s_setprio 0
	s_barrier
	s_add_i32 s43, 0, 0x18000
	v_add_u32_e32 v48, s43, v194
	s_add_i32 s75, 0, 0x1c000
	v_add_u32_e32 v49, s43, v195
	ds_read_b128 v[130:133], v48
	ds_read_b128 v[138:141], v48 offset:2048
	ds_read_b128 v[134:137], v49
	ds_read_b128 v[142:145], v49 offset:2048
	v_add_u32_e32 v48, s75, v194
	v_add_u32_e32 v49, s75, v195
	ds_read_b128 v[146:149], v48
	ds_read_b128 v[154:157], v48 offset:2048
	ds_read_b128 v[150:153], v49
	ds_read_b128 v[158:161], v49 offset:2048
	s_mov_b32 m0, s52
	v_mov_b32_e32 v176, v129
	ds_read_b128 v[48:51], v227 offset:32768
	ds_read_b128 v[162:165], v227 offset:34816
	ds_read_b128 v[52:55], v228 offset:32768
	ds_read_b128 v[166:169], v228 offset:34816
	ds_read_b128 v[196:199], v227 offset:36864
	ds_read_b128 v[232:235], v227 offset:38912
	ds_read_b128 v[200:203], v228 offset:36864
	ds_read_b128 v[236:239], v228 offset:38912
	s_mov_b32 m0, s50
	s_nop 0
	global_load_lds_dwordx4 v180, s[38:39]
	s_mov_b32 m0, s51
	s_nop 0
	global_load_lds_dwordx4 v182, s[38:39]
	s_mov_b32 m0, s52
	v_mov_b32_e32 v186, v128
	global_load_lds_dwordx4 v176, s[38:39]
	s_mov_b32 m0, s53
	s_nop 0
	global_load_lds_dwordx4 v186, s[38:39]
	s_waitcnt vmcnt(8)
	s_waitcnt lgkmcnt(0)
	s_barrier
	s_setprio 1
	s_waitcnt lgkmcnt(0)
	v_mfma_f32_16x16x128_f8f6f4 v[100:103], v[130:137], v[48:55], v[100:103]
	v_mfma_f32_16x16x128_f8f6f4 v[96:99], v[138:145], v[48:55], v[96:99]
	v_mfma_f32_16x16x128_f8f6f4 v[92:95], v[130:137], v[162:169], v[92:95]
	v_mfma_f32_16x16x128_f8f6f4 v[88:91], v[138:145], v[162:169], v[88:91]
	v_mfma_f32_16x16x128_f8f6f4 v[84:87], v[130:137], v[196:203], v[84:87]
	v_mfma_f32_16x16x128_f8f6f4 v[80:83], v[138:145], v[196:203], v[80:83]
	v_mfma_f32_16x16x128_f8f6f4 v[76:79], v[130:137], v[232:239], v[170:173]
	v_mfma_f32_16x16x128_f8f6f4 v[72:75], v[138:145], v[232:239], v[188:191]
	s_setprio 0
	s_setprio 1
	v_mfma_f32_16x16x128_f8f6f4 v[68:71], v[146:153], v[48:55], v[248:251]
	v_mfma_f32_16x16x128_f8f6f4 v[64:67], v[154:161], v[48:55], v[204:207]
	v_mfma_f32_16x16x128_f8f6f4 v[60:63], v[146:153], v[162:169], v[208:211]
	v_mfma_f32_16x16x128_f8f6f4 v[56:59], v[154:161], v[162:169], v[212:215]
	v_mfma_f32_16x16x128_f8f6f4 v[52:55], v[146:153], v[196:203], v[216:219]
	v_mfma_f32_16x16x128_f8f6f4 v[48:51], v[154:161], v[196:203], v[240:243]
	v_mfma_f32_16x16x128_f8f6f4 v[40:43], v[146:153], v[232:239], v[40:43]
	v_mfma_f32_16x16x128_f8f6f4 v[32:35], v[154:161], v[232:239], v[32:35]
	s_setprio 0
	s_barrier
	v_mov_b32_e32 v185, v177
	ds_read_b128 v[162:165], v227 offset:49152
	ds_read_b128 v[196:199], v227 offset:51200
	ds_read_b128 v[166:169], v228 offset:49152
	ds_read_b128 v[200:203], v228 offset:51200
	ds_read_b128 v[232:235], v227 offset:53248
	ds_read_b128 v[240:243], v227 offset:55296
	ds_read_b128 v[236:239], v228 offset:53248
	ds_read_b128 v[244:247], v228 offset:55296
	s_add_i32 s43, s43, s5
	s_add_u32 vcc_lo, s40, s14
	s_addc_u32 vcc_hi, s41, s15
	s_mov_b32 m0, s43
	v_mov_b32_e32 v179, v177
	global_load_lds_dwordx4 v184, vcc
	s_add_i32 m0, s43, 0x2000
	v_mov_b32_e32 v181, v177
	s_add_u32 s40, s40, 0x4080
	s_addc_u32 s41, s41, 0
	s_add_i32 s43, s75, s5
	global_load_lds_dwordx4 v178, vcc
	s_mov_b32 m0, s43
	v_mov_b32_e32 v183, v177
	global_load_lds_dwordx4 v184, s[40:41]
	s_add_i32 m0, s43, 0x2000
	s_nop 0
	global_load_lds_dwordx4 v178, s[40:41]
	s_mov_b32 m0, s62
	s_add_u32 vcc_lo, s38, s14
	s_addc_u32 vcc_hi, s39, s15
	global_load_lds_dwordx4 v180, vcc
	s_mov_b32 m0, s63
	s_nop 0
	global_load_lds_dwordx4 v182, vcc
	s_waitcnt vmcnt(8)
	s_waitcnt lgkmcnt(0)
	s_barrier
	s_setprio 1
	s_waitcnt lgkmcnt(0)
	v_mfma_f32_16x16x128_f8f6f4 v[44:47], v[130:137], v[162:169], v[44:47]
	v_mfma_f32_16x16x128_f8f6f4 v[36:39], v[138:145], v[162:169], v[36:39]
	v_mfma_f32_16x16x128_f8f6f4 v[28:31], v[130:137], v[196:203], v[28:31]
	v_mfma_f32_16x16x128_f8f6f4 v[24:27], v[138:145], v[196:203], v[24:27]
	v_mfma_f32_16x16x128_f8f6f4 v[20:23], v[130:137], v[232:239], v[20:23]
	v_mfma_f32_16x16x128_f8f6f4 v[16:19], v[138:145], v[232:239], v[16:19]
	v_mfma_f32_16x16x128_f8f6f4 v[12:15], v[130:137], v[240:247], v[12:15]
	v_mfma_f32_16x16x128_f8f6f4 v[8:11], v[138:145], v[240:247], v[8:11]
	s_setprio 0
	s_setprio 1
	v_mfma_f32_16x16x128_f8f6f4 v[4:7], v[146:153], v[162:169], v[4:7]
	v_mfma_f32_16x16x128_f8f6f4 v[0:3], v[154:161], v[162:169], v[0:3]
	v_mfma_f32_16x16x128_f8f6f4 v[104:107], v[146:153], v[196:203], v[104:107]
	v_mfma_f32_16x16x128_f8f6f4 v[108:111], v[154:161], v[196:203], v[108:111]
	v_mfma_f32_16x16x128_f8f6f4 v[112:115], v[146:153], v[232:239], v[112:115]
	v_mfma_f32_16x16x128_f8f6f4 v[116:119], v[154:161], v[232:239], v[116:119]
	v_mfma_f32_16x16x128_f8f6f4 v[120:123], v[146:153], v[240:247], v[120:123]
	v_mfma_f32_16x16x128_f8f6f4 v[124:127], v[154:161], v[240:247], v[124:127]
	s_setprio 0
	s_barrier
	s_add_i32 s42, s42, 2
	s_add_u32 s36, s36, 0x100
	s_addc_u32 s37, s37, 0
	s_cmp_gt_u32 s42, 13
	s_cbranch_scc1 .LBB0_914

.LBB0_1008:
	s_add_u32 s5, s38, 0x100
	s_addc_u32 s27, s39, 0
	s_lshl_b32 s44, s61, 8
	s_lshl_b32 s29, s61, 19
	s_bitset1_b32 s44, 7
	s_mov_b32 s45, -2
	s_mov_b64 s[38:39], 0
	s_cmp_eq_u32 s45, 12
	s_cselect_b64 s[42:43], -1, 0
	s_and_b64 s[40:41], s[36:37], s[42:43]
	s_andn2_b64 vcc, exec, s[40:41]
	v_mov_b32_e32 v131, v138
	v_mov_b32_e32 v133, v128
	v_add_u32_e32 v135, s58, v142
	s_add_u32 s64, s6, s38
	v_add_u32_e32 v137, s58, v143
	ds_read_b128 v[178:181], v135
	ds_read_b128 v[186:189], v135 offset:2048
	ds_read_b128 v[182:185], v137
	ds_read_b128 v[190:193], v137 offset:2048
	v_add_u32_e32 v135, s59, v142
	s_addc_u32 s65, s7, s39
	v_add_u32_e32 v137, s59, v143
	ds_read_b128 v[194:197], v135
	ds_read_b128 v[202:205], v135 offset:2048
	ds_read_b128 v[198:201], v137
	ds_read_b128 v[206:209], v137 offset:2048
	s_add_u32 s66, s64, 0x5e000100
	s_addc_u32 s67, s65, 0
	s_and_b64 s[40:41], s[42:43], exec
	s_cselect_b32 s41, s11, s67
	s_cselect_b32 s40, s10, s66
	s_add_u32 s66, s5, s38
	s_addc_u32 s67, s27, s39
	s_and_b64 s[42:43], s[42:43], exec
	s_cselect_b32 s43, s35, s67
	s_cselect_b32 s42, s34, s66
	ds_read_b128 v[210:213], v175
	ds_read_b128 v[218:221], v175 offset:2048
	ds_read_b128 v[214:217], v176
	ds_read_b128 v[222:225], v176 offset:2048
	ds_read_b128 v[226:229], v175 offset:4096
	ds_read_b128 v[234:237], v175 offset:6144
	ds_read_b128 v[230:233], v176 offset:4096
	ds_read_b128 v[238:241], v176 offset:6144
	s_add_i32 m0, s1, 0xc000
	s_add_u32 vcc_lo, s64, s16
	s_addc_u32 vcc_hi, s65, s17
	global_load_lds_dwordx4 v128, vcc
	v_mov_b32_e32 v139, v129
	s_add_i32 m0, s1, 0xe000
	s_nop 0
	global_load_lds_dwordx4 v138, vcc
	s_waitcnt vmcnt(8)
	s_waitcnt lgkmcnt(0)
	s_barrier
	s_setprio 1
	s_waitcnt lgkmcnt(0)
	v_mfma_f32_16x16x128_f8f6f4 v[100:103], v[178:185], v[210:217], 0
	v_mfma_f32_16x16x128_f8f6f4 v[96:99], v[186:193], v[210:217], 0
	v_mfma_f32_16x16x128_f8f6f4 v[92:95], v[178:185], v[218:225], 0
	v_mfma_f32_16x16x128_f8f6f4 v[88:91], v[186:193], v[218:225], 0
	v_mfma_f32_16x16x128_f8f6f4 v[84:87], v[178:185], v[226:233], 0
	v_mfma_f32_16x16x128_f8f6f4 v[80:83], v[186:193], v[226:233], 0
	v_mfma_f32_16x16x128_f8f6f4 v[242:245], v[178:185], v[234:241], 0
	v_mfma_f32_16x16x128_f8f6f4 v[246:249], v[186:193], v[234:241], 0
	s_setprio 0
	s_setprio 1
	v_mfma_f32_16x16x128_f8f6f4 v[40:43], v[194:201], v[234:241], 0
	v_mfma_f32_16x16x128_f8f6f4 v[32:35], v[202:209], v[234:241], 0
	v_mfma_f32_16x16x128_f8f6f4 v[250:253], v[194:201], v[210:217], 0
	v_mfma_f32_16x16x128_f8f6f4 v[144:147], v[202:209], v[210:217], 0
	v_mfma_f32_16x16x128_f8f6f4 v[148:151], v[194:201], v[218:225], 0
	v_mfma_f32_16x16x128_f8f6f4 v[152:155], v[202:209], v[218:225], 0
	v_mfma_f32_16x16x128_f8f6f4 v[156:159], v[194:201], v[226:233], 0
	v_mfma_f32_16x16x128_f8f6f4 v[160:163], v[202:209], v[226:233], 0
	s_setprio 0
	s_barrier
	s_add_i32 s64, s58, s48
	s_mov_b32 m0, s64
	s_nop 2
	ds_read_b128 v[48:51], v175 offset:16384
	ds_read_b128 v[56:59], v175 offset:18432
	ds_read_b128 v[52:55], v176 offset:16384
	ds_read_b128 v[60:63], v176 offset:18432
	ds_read_b128 v[64:67], v175 offset:20480
	ds_read_b128 v[72:75], v175 offset:22528
	ds_read_b128 v[68:71], v176 offset:20480
	ds_read_b128 v[76:79], v176 offset:22528
	s_nop 0
	global_load_lds_dwordx4 v136, s[42:43]
	s_add_i32 m0, s64, 0x2000
	s_add_u32 s64, s42, 0x4000
	s_addc_u32 s65, s43, 0
	s_add_i32 s66, s59, s48
	s_nop 0
	global_load_lds_dwordx4 v130, s[42:43]
	s_mov_b32 m0, s66
	s_nop 0
	global_load_lds_dwordx4 v136, s[64:65]
	s_add_i32 m0, s66, 0x2000
	s_nop 0
	global_load_lds_dwordx4 v130, s[64:65]
	s_waitcnt vmcnt(6)
	s_waitcnt lgkmcnt(0)
	s_barrier
	s_setprio 1
	s_waitcnt lgkmcnt(0)
	v_mfma_f32_16x16x128_f8f6f4 v[44:47], v[178:185], v[48:55], 0
	v_mfma_f32_16x16x128_f8f6f4 v[36:39], v[186:193], v[48:55], 0
	v_mfma_f32_16x16x128_f8f6f4 v[28:31], v[178:185], v[56:63], 0
	v_mfma_f32_16x16x128_f8f6f4 v[24:27], v[186:193], v[56:63], 0
	v_mfma_f32_16x16x128_f8f6f4 v[20:23], v[178:185], v[64:71], 0
	v_mfma_f32_16x16x128_f8f6f4 v[16:19], v[186:193], v[64:71], 0
	v_mfma_f32_16x16x128_f8f6f4 v[12:15], v[178:185], v[72:79], 0
	v_mfma_f32_16x16x128_f8f6f4 v[8:11], v[186:193], v[72:79], 0
	s_setprio 0
	s_setprio 1
	v_mfma_f32_16x16x128_f8f6f4 v[4:7], v[194:201], v[48:55], 0
	v_mfma_f32_16x16x128_f8f6f4 v[0:3], v[202:209], v[48:55], 0
	v_mfma_f32_16x16x128_f8f6f4 v[104:107], v[194:201], v[56:63], 0
	v_mfma_f32_16x16x128_f8f6f4 v[108:111], v[202:209], v[56:63], 0
	v_mfma_f32_16x16x128_f8f6f4 v[112:115], v[194:201], v[64:71], 0
	v_mfma_f32_16x16x128_f8f6f4 v[116:119], v[202:209], v[64:71], 0
	v_mfma_f32_16x16x128_f8f6f4 v[120:123], v[194:201], v[72:79], 0
	v_mfma_f32_16x16x128_f8f6f4 v[124:127], v[202:209], v[72:79], 0
	s_setprio 0
	s_barrier
	s_add_i32 s64, 0, 0x18000
	v_add_u32_e32 v48, s64, v142
	s_add_i32 s65, 0, 0x1c000
	v_add_u32_e32 v49, s64, v143
	ds_read_b128 v[178:181], v48
	ds_read_b128 v[186:189], v48 offset:2048
	ds_read_b128 v[182:185], v49
	ds_read_b128 v[190:193], v49 offset:2048
	v_add_u32_e32 v48, s65, v142
	v_add_u32_e32 v49, s65, v143
	ds_read_b128 v[194:197], v48
	ds_read_b128 v[202:205], v48 offset:2048
	ds_read_b128 v[198:201], v49
	ds_read_b128 v[206:209], v49 offset:2048
	s_mov_b32 m0, s50
	v_mov_b32_e32 v128, v133
	ds_read_b128 v[48:51], v175 offset:32768
	ds_read_b128 v[210:213], v175 offset:34816
	ds_read_b128 v[52:55], v176 offset:32768
	ds_read_b128 v[214:217], v176 offset:34816
	ds_read_b128 v[218:221], v175 offset:36864
	ds_read_b128 v[226:229], v175 offset:38912
	ds_read_b128 v[222:225], v176 offset:36864
	ds_read_b128 v[230:233], v176 offset:38912
	s_mov_b32 m0, s1
	s_nop 0
	global_load_lds_dwordx4 v132, s[40:41]
	s_mov_b32 m0, s49
	s_nop 0
	global_load_lds_dwordx4 v134, s[40:41]
	s_mov_b32 m0, s50
	v_mov_b32_e32 v138, v131
	global_load_lds_dwordx4 v128, s[40:41]
	s_mov_b32 m0, s51
	s_nop 0
	global_load_lds_dwordx4 v138, s[40:41]
	s_waitcnt vmcnt(8)
	s_waitcnt lgkmcnt(0)
	s_barrier
	s_setprio 1
	s_waitcnt lgkmcnt(0)
	v_mfma_f32_16x16x128_f8f6f4 v[100:103], v[178:185], v[48:55], v[100:103]
	v_mfma_f32_16x16x128_f8f6f4 v[96:99], v[186:193], v[48:55], v[96:99]
	v_mfma_f32_16x16x128_f8f6f4 v[92:95], v[178:185], v[210:217], v[92:95]
	v_mfma_f32_16x16x128_f8f6f4 v[88:91], v[186:193], v[210:217], v[88:91]
	v_mfma_f32_16x16x128_f8f6f4 v[84:87], v[178:185], v[218:225], v[84:87]
	v_mfma_f32_16x16x128_f8f6f4 v[80:83], v[186:193], v[218:225], v[80:83]
	v_mfma_f32_16x16x128_f8f6f4 v[76:79], v[178:185], v[226:233], v[242:245]
	v_mfma_f32_16x16x128_f8f6f4 v[72:75], v[186:193], v[226:233], v[246:249]
	s_setprio 0
	s_setprio 1
	v_mfma_f32_16x16x128_f8f6f4 v[68:71], v[194:201], v[48:55], v[250:253]
	v_mfma_f32_16x16x128_f8f6f4 v[64:67], v[202:209], v[48:55], v[144:147]
	v_mfma_f32_16x16x128_f8f6f4 v[60:63], v[194:201], v[210:217], v[148:151]
	v_mfma_f32_16x16x128_f8f6f4 v[56:59], v[202:209], v[210:217], v[152:155]
	v_mfma_f32_16x16x128_f8f6f4 v[52:55], v[194:201], v[218:225], v[156:159]
	v_mfma_f32_16x16x128_f8f6f4 v[48:51], v[202:209], v[218:225], v[160:163]
	v_mfma_f32_16x16x128_f8f6f4 v[40:43], v[194:201], v[226:233], v[40:43]
	v_mfma_f32_16x16x128_f8f6f4 v[32:35], v[202:209], v[226:233], v[32:35]
	s_setprio 0
	s_barrier
	v_mov_b32_e32 v137, v129
	ds_read_b128 v[210:213], v175 offset:49152
	ds_read_b128 v[218:221], v175 offset:51200
	ds_read_b128 v[214:217], v176 offset:49152
	ds_read_b128 v[222:225], v176 offset:51200
	ds_read_b128 v[226:229], v175 offset:53248
	ds_read_b128 v[234:237], v175 offset:55296
	ds_read_b128 v[230:233], v176 offset:53248
	ds_read_b128 v[238:241], v176 offset:55296
	s_add_i32 s64, s64, s48
	s_add_u32 vcc_lo, s42, s14
	s_addc_u32 vcc_hi, s43, s15
	s_mov_b32 m0, s64
	v_mov_b32_e32 v131, v129
	global_load_lds_dwordx4 v136, vcc
	s_add_i32 m0, s64, 0x2000
	v_mov_b32_e32 v133, v129
	s_add_u32 s42, s42, 0x4080
	s_addc_u32 s43, s43, 0
	s_add_i32 s64, s65, s48
	global_load_lds_dwordx4 v130, vcc
	s_mov_b32 m0, s64
	v_mov_b32_e32 v135, v129
	global_load_lds_dwordx4 v136, s[42:43]
	s_add_i32 m0, s64, 0x2000
	s_nop 0
	global_load_lds_dwordx4 v130, s[42:43]
	s_mov_b32 m0, s53
	s_add_u32 vcc_lo, s40, s14
	s_addc_u32 vcc_hi, s41, s15
	global_load_lds_dwordx4 v132, vcc
	s_mov_b32 m0, s54
	s_nop 0
	global_load_lds_dwordx4 v134, vcc
	s_waitcnt vmcnt(8)
	s_waitcnt lgkmcnt(0)
	s_barrier
	s_setprio 1
	s_waitcnt lgkmcnt(0)
	v_mfma_f32_16x16x128_f8f6f4 v[44:47], v[178:185], v[210:217], v[44:47]
	v_mfma_f32_16x16x128_f8f6f4 v[36:39], v[186:193], v[210:217], v[36:39]
	v_mfma_f32_16x16x128_f8f6f4 v[28:31], v[178:185], v[218:225], v[28:31]
	v_mfma_f32_16x16x128_f8f6f4 v[24:27], v[186:193], v[218:225], v[24:27]
	v_mfma_f32_16x16x128_f8f6f4 v[20:23], v[178:185], v[226:233], v[20:23]
	v_mfma_f32_16x16x128_f8f6f4 v[16:19], v[186:193], v[226:233], v[16:19]
	v_mfma_f32_16x16x128_f8f6f4 v[12:15], v[178:185], v[234:241], v[12:15]
	v_mfma_f32_16x16x128_f8f6f4 v[8:11], v[186:193], v[234:241], v[8:11]
	s_setprio 0
	s_setprio 1
	v_mfma_f32_16x16x128_f8f6f4 v[4:7], v[194:201], v[210:217], v[4:7]
	v_mfma_f32_16x16x128_f8f6f4 v[0:3], v[202:209], v[210:217], v[0:3]
	v_mfma_f32_16x16x128_f8f6f4 v[104:107], v[194:201], v[218:225], v[104:107]
	v_mfma_f32_16x16x128_f8f6f4 v[108:111], v[202:209], v[218:225], v[108:111]
	v_mfma_f32_16x16x128_f8f6f4 v[112:115], v[194:201], v[226:233], v[112:115]
	v_mfma_f32_16x16x128_f8f6f4 v[116:119], v[202:209], v[226:233], v[116:119]
	v_mfma_f32_16x16x128_f8f6f4 v[120:123], v[194:201], v[234:241], v[120:123]
	v_mfma_f32_16x16x128_f8f6f4 v[124:127], v[202:209], v[234:241], v[124:127]
	s_setprio 0
	s_barrier
	s_add_i32 s45, s45, 2
	s_add_u32 s38, s38, 0x100
	s_addc_u32 s39, s39, 0
	s_branch .LBB0_1010
.LBB0_1009:
	v_add_u32_e32 v135, s58, v142
	s_add_u32 s64, s6, s38
	v_add_u32_e32 v137, s58, v143
	ds_read_b128 v[178:181], v135
	ds_read_b128 v[186:189], v135 offset:2048
	ds_read_b128 v[182:185], v137
	ds_read_b128 v[190:193], v137 offset:2048
	v_add_u32_e32 v135, s59, v142
	s_addc_u32 s65, s7, s39
	v_add_u32_e32 v137, s59, v143
	ds_read_b128 v[194:197], v135
	ds_read_b128 v[202:205], v135 offset:2048
	ds_read_b128 v[198:201], v137
	ds_read_b128 v[206:209], v137 offset:2048
	s_add_u32 s66, s64, 0x5e000100
	s_addc_u32 s67, s65, 0
	s_and_b64 s[40:41], s[42:43], exec
	s_cselect_b32 s41, s11, s67
	s_cselect_b32 s40, s10, s66
	s_add_u32 s66, s5, s38
	s_addc_u32 s67, s27, s39
	s_and_b64 s[42:43], s[42:43], exec
	s_cselect_b32 s43, s35, s67
	s_cselect_b32 s42, s34, s66
	ds_read_b128 v[210:213], v175
	ds_read_b128 v[218:221], v175 offset:2048
	ds_read_b128 v[214:217], v176
	ds_read_b128 v[222:225], v176 offset:2048
	ds_read_b128 v[226:229], v175 offset:4096
	ds_read_b128 v[234:237], v175 offset:6144
	ds_read_b128 v[230:233], v176 offset:4096
	ds_read_b128 v[238:241], v176 offset:6144
	s_add_i32 m0, s1, 0xc000
	s_add_u32 vcc_lo, s64, s16
	s_addc_u32 vcc_hi, s65, s17
	global_load_lds_dwordx4 v128, vcc
	v_mov_b32_e32 v139, v129
	s_add_i32 m0, s1, 0xe000
	s_nop 0
	global_load_lds_dwordx4 v138, vcc
	s_waitcnt vmcnt(8)
	s_waitcnt lgkmcnt(0)
	s_barrier
	s_setprio 1
	s_waitcnt lgkmcnt(0)
	v_mfma_f32_16x16x128_f8f6f4 v[100:103], v[178:185], v[210:217], v[100:103]
	v_mfma_f32_16x16x128_f8f6f4 v[96:99], v[186:193], v[210:217], v[96:99]
	v_mfma_f32_16x16x128_f8f6f4 v[92:95], v[178:185], v[218:225], v[92:95]
	v_mfma_f32_16x16x128_f8f6f4 v[88:91], v[186:193], v[218:225], v[88:91]
	v_mfma_f32_16x16x128_f8f6f4 v[84:87], v[178:185], v[226:233], v[84:87]
	v_mfma_f32_16x16x128_f8f6f4 v[80:83], v[186:193], v[226:233], v[80:83]
	v_mfma_f32_16x16x128_f8f6f4 v[242:245], v[178:185], v[234:241], v[76:79]
	v_mfma_f32_16x16x128_f8f6f4 v[246:249], v[186:193], v[234:241], v[72:75]
	s_setprio 0
	s_setprio 1
	v_mfma_f32_16x16x128_f8f6f4 v[40:43], v[194:201], v[234:241], v[40:43]
	v_mfma_f32_16x16x128_f8f6f4 v[32:35], v[202:209], v[234:241], v[32:35]
	v_mfma_f32_16x16x128_f8f6f4 v[250:253], v[194:201], v[210:217], v[68:71]
	v_mfma_f32_16x16x128_f8f6f4 v[144:147], v[202:209], v[210:217], v[64:67]
	v_mfma_f32_16x16x128_f8f6f4 v[148:151], v[194:201], v[218:225], v[60:63]
	v_mfma_f32_16x16x128_f8f6f4 v[152:155], v[202:209], v[218:225], v[56:59]
	v_mfma_f32_16x16x128_f8f6f4 v[156:159], v[194:201], v[226:233], v[52:55]
	v_mfma_f32_16x16x128_f8f6f4 v[160:163], v[202:209], v[226:233], v[48:51]
	s_setprio 0
	s_barrier
	s_add_i32 s64, s58, s48
	s_mov_b32 m0, s64
	s_nop 2
	ds_read_b128 v[48:51], v175 offset:16384
	ds_read_b128 v[56:59], v175 offset:18432
	ds_read_b128 v[52:55], v176 offset:16384
	ds_read_b128 v[60:63], v176 offset:18432
	ds_read_b128 v[64:67], v175 offset:20480
	ds_read_b128 v[72:75], v175 offset:22528
	ds_read_b128 v[68:71], v176 offset:20480
	ds_read_b128 v[76:79], v176 offset:22528
	s_nop 0
	global_load_lds_dwordx4 v136, s[42:43]
	s_add_i32 m0, s64, 0x2000
	s_add_u32 s64, s42, 0x4000
	s_addc_u32 s65, s43, 0
	s_add_i32 s66, s59, s48
	s_nop 0
	global_load_lds_dwordx4 v130, s[42:43]
	s_mov_b32 m0, s66
	s_nop 0
	global_load_lds_dwordx4 v136, s[64:65]
	s_add_i32 m0, s66, 0x2000
	s_nop 0
	global_load_lds_dwordx4 v130, s[64:65]
	s_waitcnt vmcnt(6)
	s_waitcnt lgkmcnt(0)
	s_barrier
	s_setprio 1
	s_waitcnt lgkmcnt(0)
	v_mfma_f32_16x16x128_f8f6f4 v[44:47], v[178:185], v[48:55], v[44:47]
	v_mfma_f32_16x16x128_f8f6f4 v[36:39], v[186:193], v[48:55], v[36:39]
	v_mfma_f32_16x16x128_f8f6f4 v[28:31], v[178:185], v[56:63], v[28:31]
	v_mfma_f32_16x16x128_f8f6f4 v[24:27], v[186:193], v[56:63], v[24:27]
	v_mfma_f32_16x16x128_f8f6f4 v[20:23], v[178:185], v[64:71], v[20:23]
	v_mfma_f32_16x16x128_f8f6f4 v[16:19], v[186:193], v[64:71], v[16:19]
	v_mfma_f32_16x16x128_f8f6f4 v[12:15], v[178:185], v[72:79], v[12:15]
	v_mfma_f32_16x16x128_f8f6f4 v[8:11], v[186:193], v[72:79], v[8:11]
	s_setprio 0
	s_setprio 1
	v_mfma_f32_16x16x128_f8f6f4 v[4:7], v[194:201], v[48:55], v[4:7]
	v_mfma_f32_16x16x128_f8f6f4 v[0:3], v[202:209], v[48:55], v[0:3]
	v_mfma_f32_16x16x128_f8f6f4 v[104:107], v[194:201], v[56:63], v[104:107]
	v_mfma_f32_16x16x128_f8f6f4 v[108:111], v[202:209], v[56:63], v[108:111]
	v_mfma_f32_16x16x128_f8f6f4 v[112:115], v[194:201], v[64:71], v[112:115]
	v_mfma_f32_16x16x128_f8f6f4 v[116:119], v[202:209], v[64:71], v[116:119]
	v_mfma_f32_16x16x128_f8f6f4 v[120:123], v[194:201], v[72:79], v[120:123]
	v_mfma_f32_16x16x128_f8f6f4 v[124:127], v[202:209], v[72:79], v[124:127]
	s_setprio 0
	s_barrier
	s_add_i32 s64, 0, 0x18000
	v_add_u32_e32 v48, s64, v142
	s_add_i32 s65, 0, 0x1c000
	v_add_u32_e32 v49, s64, v143
	ds_read_b128 v[178:181], v48
	ds_read_b128 v[186:189], v48 offset:2048
	ds_read_b128 v[182:185], v49
	ds_read_b128 v[190:193], v49 offset:2048
	v_add_u32_e32 v48, s65, v142
	v_add_u32_e32 v49, s65, v143
	ds_read_b128 v[194:197], v48
	ds_read_b128 v[202:205], v48 offset:2048
	ds_read_b128 v[198:201], v49
	ds_read_b128 v[206:209], v49 offset:2048
	s_mov_b32 m0, s50
	v_mov_b32_e32 v128, v133
	ds_read_b128 v[48:51], v175 offset:32768
	ds_read_b128 v[210:213], v175 offset:34816
	ds_read_b128 v[52:55], v176 offset:32768
	ds_read_b128 v[214:217], v176 offset:34816
	ds_read_b128 v[218:221], v175 offset:36864
	ds_read_b128 v[226:229], v175 offset:38912
	ds_read_b128 v[222:225], v176 offset:36864
	ds_read_b128 v[230:233], v176 offset:38912
	s_mov_b32 m0, s1
	s_nop 0
	global_load_lds_dwordx4 v132, s[40:41]
	s_mov_b32 m0, s49
	s_nop 0
	global_load_lds_dwordx4 v134, s[40:41]
	s_mov_b32 m0, s50
	v_mov_b32_e32 v138, v131
	global_load_lds_dwordx4 v128, s[40:41]
	s_mov_b32 m0, s51
	s_nop 0
	global_load_lds_dwordx4 v138, s[40:41]
	s_waitcnt vmcnt(8)
	s_waitcnt lgkmcnt(0)
	s_barrier
	s_setprio 1
	s_waitcnt lgkmcnt(0)
	v_mfma_f32_16x16x128_f8f6f4 v[100:103], v[178:185], v[48:55], v[100:103]
	v_mfma_f32_16x16x128_f8f6f4 v[96:99], v[186:193], v[48:55], v[96:99]
	v_mfma_f32_16x16x128_f8f6f4 v[92:95], v[178:185], v[210:217], v[92:95]
	v_mfma_f32_16x16x128_f8f6f4 v[88:91], v[186:193], v[210:217], v[88:91]
	v_mfma_f32_16x16x128_f8f6f4 v[84:87], v[178:185], v[218:225], v[84:87]
	v_mfma_f32_16x16x128_f8f6f4 v[80:83], v[186:193], v[218:225], v[80:83]
	v_mfma_f32_16x16x128_f8f6f4 v[76:79], v[178:185], v[226:233], v[242:245]
	v_mfma_f32_16x16x128_f8f6f4 v[72:75], v[186:193], v[226:233], v[246:249]
	s_setprio 0
	s_setprio 1
	v_mfma_f32_16x16x128_f8f6f4 v[68:71], v[194:201], v[48:55], v[250:253]
	v_mfma_f32_16x16x128_f8f6f4 v[64:67], v[202:209], v[48:55], v[144:147]
	v_mfma_f32_16x16x128_f8f6f4 v[60:63], v[194:201], v[210:217], v[148:151]
	v_mfma_f32_16x16x128_f8f6f4 v[56:59], v[202:209], v[210:217], v[152:155]
	v_mfma_f32_16x16x128_f8f6f4 v[52:55], v[194:201], v[218:225], v[156:159]
	v_mfma_f32_16x16x128_f8f6f4 v[48:51], v[202:209], v[218:225], v[160:163]
	v_mfma_f32_16x16x128_f8f6f4 v[40:43], v[194:201], v[226:233], v[40:43]
	v_mfma_f32_16x16x128_f8f6f4 v[32:35], v[202:209], v[226:233], v[32:35]
	s_setprio 0
	s_barrier
	v_mov_b32_e32 v137, v129
	ds_read_b128 v[210:213], v175 offset:49152
	ds_read_b128 v[218:221], v175 offset:51200
	ds_read_b128 v[214:217], v176 offset:49152
	ds_read_b128 v[222:225], v176 offset:51200
	ds_read_b128 v[226:229], v175 offset:53248
	ds_read_b128 v[234:237], v175 offset:55296
	ds_read_b128 v[230:233], v176 offset:53248
	ds_read_b128 v[238:241], v176 offset:55296
	s_add_i32 s64, s64, s48
	s_add_u32 vcc_lo, s42, s14
	s_addc_u32 vcc_hi, s43, s15
	s_mov_b32 m0, s64
	v_mov_b32_e32 v131, v129
	global_load_lds_dwordx4 v136, vcc
	s_add_i32 m0, s64, 0x2000
	v_mov_b32_e32 v133, v129
	s_add_u32 s42, s42, 0x4080
	s_addc_u32 s43, s43, 0
	s_add_i32 s64, s65, s48
	global_load_lds_dwordx4 v130, vcc
	s_mov_b32 m0, s64
	v_mov_b32_e32 v135, v129
	global_load_lds_dwordx4 v136, s[42:43]
	s_add_i32 m0, s64, 0x2000
	s_nop 0
	global_load_lds_dwordx4 v130, s[42:43]
	s_mov_b32 m0, s53
	s_add_u32 vcc_lo, s40, s14
	s_addc_u32 vcc_hi, s41, s15
	global_load_lds_dwordx4 v132, vcc
	s_mov_b32 m0, s54
	s_nop 0
	global_load_lds_dwordx4 v134, vcc
	s_waitcnt vmcnt(8)
	s_waitcnt lgkmcnt(0)
	s_barrier
	s_setprio 1
	s_waitcnt lgkmcnt(0)
	v_mfma_f32_16x16x128_f8f6f4 v[44:47], v[178:185], v[210:217], v[44:47]
	v_mfma_f32_16x16x128_f8f6f4 v[36:39], v[186:193], v[210:217], v[36:39]
	v_mfma_f32_16x16x128_f8f6f4 v[28:31], v[178:185], v[218:225], v[28:31]
	v_mfma_f32_16x16x128_f8f6f4 v[24:27], v[186:193], v[218:225], v[24:27]
	v_mfma_f32_16x16x128_f8f6f4 v[20:23], v[178:185], v[226:233], v[20:23]
	v_mfma_f32_16x16x128_f8f6f4 v[16:19], v[186:193], v[226:233], v[16:19]
	v_mfma_f32_16x16x128_f8f6f4 v[12:15], v[178:185], v[234:241], v[12:15]
	v_mfma_f32_16x16x128_f8f6f4 v[8:11], v[186:193], v[234:241], v[8:11]
	s_setprio 0
	s_setprio 1
	v_mfma_f32_16x16x128_f8f6f4 v[4:7], v[194:201], v[210:217], v[4:7]
	v_mfma_f32_16x16x128_f8f6f4 v[0:3], v[202:209], v[210:217], v[0:3]
	v_mfma_f32_16x16x128_f8f6f4 v[104:107], v[194:201], v[218:225], v[104:107]
	v_mfma_f32_16x16x128_f8f6f4 v[108:111], v[202:209], v[218:225], v[108:111]
	v_mfma_f32_16x16x128_f8f6f4 v[112:115], v[194:201], v[226:233], v[112:115]
	v_mfma_f32_16x16x128_f8f6f4 v[116:119], v[202:209], v[226:233], v[116:119]
	v_mfma_f32_16x16x128_f8f6f4 v[120:123], v[194:201], v[234:241], v[120:123]
	v_mfma_f32_16x16x128_f8f6f4 v[124:127], v[202:209], v[234:241], v[124:127]
	s_setprio 0
	s_barrier
	s_add_i32 s45, s45, 2
	s_add_u32 s38, s38, 0x100
	s_addc_u32 s39, s39, 0
	s_cmp_gt_u32 s45, 13
	s_cbranch_scc1 .LBB0_1012
